# SwiGLU H8 stores carry the nt (streaming) cache hint
# speedup vs baseline: 1.0015x; 1.0015x over previous
; __device__ __forceinline__ float rstd_fin4(const f32x4 a) { float s = (a[0] + a[1]) + (a[2] + a[3]); s += __shfl_xor(s, 16); s += __shfl_xor(s, 32); return __builtin_amdgcn_rsqf(s * (1.f / 1024.f) + 1e-6f); }
;     __device__ __forceinline__ void operator()(const f32x4 (&acc)[2][2][4][2], const Unit& u, int wr, int wc, int fr, int fq) const {
;     ...
;         const int row0 = u.pm * BM + wr * 64 + fr;
;         unsigned char* const hb = (unsigned char*)H + (size_t)(u.pm * (FFH / 128) + u.pn + pn0) * 32768 + (((wr * 4 + wc) * 8) * 64 + (fq >> 1) * 32 + fr * 2 + (fq & 1)) * 8;
;         f32x4 pa[2][4];
; #pragma unroll
;         for (int ai = 0; ai < 2; ++ai)
; #pragma unroll
;             for (int m = 0; m < 4; ++m) pa[ai][m] = rstd_ld4(ss, row0 + ai * HALF + m * 16, fq);
; #pragma unroll
;         for (int ai = 0; ai < 2; ++ai)
; #pragma unroll
;             for (int m = 0; m < 4; ++m) { const float rs = rstd_fin4(pa[ai][m]) * sc;
;                 const float rsl = rs * 1.4426950408889634f, rsu = rs * 0.6931471805599453f;
;                 f32x4 h0, h1;
; #pragma unroll
;                 for (int n = 0; n < 2; ++n) { const f32x4 G = acc[ai][0][m][n], U = acc[ai][1][m][n]; f32x4 hv;
; #pragma unroll
;                     for (int q = 0; q < 2; ++q) { const f32x2 g2 = (f32x2){G[2 * q], G[2 * q + 1]} * rsl, u2 = (f32x2){U[2 * q], U[2 * q + 1]} * rsu;
;                         f32x2 r2; r2.x = __builtin_amdgcn_rcpf(1.f + __builtin_amdgcn_exp2f(-g2.x)); r2.y = __builtin_amdgcn_rcpf(1.f + __builtin_amdgcn_exp2f(-g2.y));
.LBB0_434:
	s_lshl_b32 s4, s71, 8
	v_mov_b32_e32 v142, v1
	v_mov_b32_e32 v143, v164
	s_add_i32 s4, s4, s47
	v_and_b32_e32 v145, 64, v246
	v_add_u32_e32 v132, s4, v142
	v_lshlrev_b32_e32 v134, 2, v143
	v_ashrrev_i32_e32 v135, 31, v134
	v_ashrrev_i32_e32 v133, 31, v132
	v_lshl_add_u64 v[134:135], v[134:135], 2, s[48:49]
	v_lshlrev_b64 v[132:133], 6, v[132:133]
	v_lshl_add_u64 v[140:141], v[134:135], 0, v[132:133]
	global_load_dwordx4 v[132:135], v[140:141], off
	global_load_dwordx4 v[136:139], v[140:141], off offset:1024
	global_load_dwordx4 v[170:173], v[140:141], off offset:2048
	global_load_dwordx4 v[148:151], v[140:141], off offset:3072
	v_xor_b32_e32 v144, 16, v246
	v_add_u32_e32 v145, 64, v145
	v_xor_b32_e32 v146, 32, v246
	v_cmp_lt_i32_e32 vcc, v144, v145
	s_mul_i32 s4, s71, 22
	s_add_i32 s4, s4, s70
	v_cndmask_b32_e32 v144, v246, v144, vcc
	v_cmp_lt_i32_e32 vcc, v146, v145
	v_lshlrev_b32_e32 v168, 2, v144
	s_ashr_i32 s5, s4, 31
	v_cndmask_b32_e32 v145, v246, v146, vcc
	v_lshlrev_b32_e32 v167, 2, v145
	v_lshlrev_b32_e32 v147, 4, v143
	v_lshl_add_u32 v142, v142, 1, s68
	s_lshl_b64 s[4:5], s[4:5], 15
	v_and_b32_e32 v146, 0x1fffffe0, v147
	v_and_or_b32 v142, v143, 1, v142
	v_add_lshl_u32 v142, v142, v146, 3
	s_add_u32 s4, s22, s4
	v_ashrrev_i32_e32 v143, 31, v142
	s_addc_u32 s5, s23, s5
	v_lshl_add_u64 v[162:163], s[4:5], 0, v[142:143]
	v_mov_b32_e32 v174, v3
	v_mov_b32_e32 v175, v3
	s_mov_b64 s[4:5], -1
	s_waitcnt vmcnt(0)
	v_mov_b32_e32 v144, v133
	v_mov_b32_e32 v145, v134
	v_mov_b32_e32 v133, v135
	v_mov_b32_e32 v134, v137
	v_mov_b32_e32 v135, v138
	v_mov_b32_e32 v137, v139
	v_pk_add_f32 v[134:135], v[134:135], v[136:137]
	v_pk_add_f32 v[132:133], v[144:145], v[132:133]
	v_add_f32_e32 v134, v134, v135
	v_add_f32_e32 v136, v132, v133
	ds_bpermute_b32 v137, v168, v134
	ds_bpermute_b32 v135, v168, v136
	v_add_co_u32_e32 v132, vcc, s88, v140
	s_waitcnt lgkmcnt(1)
	v_add_f32_e32 v134, v134, v137
	s_waitcnt lgkmcnt(0)
	v_add_f32_e32 v135, v136, v135
	ds_bpermute_b32 v137, v167, v134
	ds_bpermute_b32 v136, v167, v135
	v_addc_co_u32_e32 v133, vcc, 0, v141, vcc
	global_load_dwordx4 v[144:147], v[132:133], off
	global_load_dwordx4 v[140:143], v[132:133], off offset:1024
	s_waitcnt lgkmcnt(1)
	v_add_f32_e32 v134, v134, v137
	s_waitcnt lgkmcnt(0)
	v_add_f32_e32 v135, v135, v136
	v_fmamk_f32 v134, v134, 0x3a800000, v227
	v_fmamk_f32 v135, v135, 0x3a800000, v227
	v_rsq_f32_e32 v177, v134
	v_rsq_f32_e32 v169, v135
	global_load_dwordx4 v[136:139], v[132:133], off offset:2048
	s_nop 0
	global_load_dwordx4 v[132:135], v[132:133], off offset:3072
	s_andn2_b64 vcc, exec, s[38:39]
	v_mul_f32_e32 v180, 0x3fb8aa3b, v177
	v_mul_f32_e32 v182, 0x3f317218, v177
	v_mul_f32_e32 v176, 0x3fb8aa3b, v169
	v_mul_f32_e32 v178, 0x3f317218, v169
	v_pk_mul_f32 v[112:113], v[112:113], v[180:181] op_sel_hi:[1,0]
	v_pk_mul_f32 v[104:105], v[104:105], v[182:183] op_sel_hi:[1,0]
	v_pk_mul_f32 v[128:129], v[128:129], v[176:177] op_sel_hi:[1,0]
	v_pk_mul_f32 v[120:121], v[120:121], v[178:179] op_sel_hi:[1,0]
	v_pk_mul_f32 v[130:131], v[130:131], v[176:177] op_sel_hi:[1,0]
	v_pk_mul_f32 v[122:123], v[122:123], v[178:179] op_sel_hi:[1,0]
	v_pk_mul_f32 v[124:125], v[124:125], v[176:177] op_sel_hi:[1,0]
	v_pk_mul_f32 v[116:117], v[116:117], v[178:179] op_sel_hi:[1,0]
	v_pk_mul_f32 v[126:127], v[126:127], v[176:177] op_sel_hi:[1,0]
	v_pk_mul_f32 v[118:119], v[118:119], v[178:179] op_sel_hi:[1,0]
	v_exp_f32_e64 v177, -v112
	v_exp_f32_e64 v178, -v113
	v_pk_mul_f32 v[104:105], v[112:113], v[104:105]
	v_pk_mul_f32 v[112:113], v[114:115], v[180:181] op_sel_hi:[1,0]
	v_pk_mul_f32 v[106:107], v[106:107], v[182:183] op_sel_hi:[1,0]
	v_exp_f32_e64 v114, -v112
	v_exp_f32_e64 v115, -v113
	v_pk_mul_f32 v[108:109], v[108:109], v[180:181] op_sel_hi:[1,0]
	v_pk_mul_f32 v[106:107], v[112:113], v[106:107]
	v_add_f32_e32 v114, 1.0, v114
	v_add_f32_e32 v115, 1.0, v115
	v_exp_f32_e64 v112, -v108
	v_exp_f32_e64 v113, -v109
	v_rcp_f32_e32 v114, v114
	v_rcp_f32_e32 v115, v115
	v_exp_f32_e64 v169, -v128
	v_exp_f32_e64 v176, -v129
	v_pk_mul_f32 v[120:121], v[128:129], v[120:121]
	v_exp_f32_e64 v128, -v130
	v_exp_f32_e64 v129, -v131
	v_pk_mul_f32 v[122:123], v[130:131], v[122:123]
	v_exp_f32_e64 v130, -v124
	v_exp_f32_e64 v131, -v125
	v_pk_mul_f32 v[116:117], v[124:125], v[116:117]
	v_exp_f32_e64 v124, -v126
	v_exp_f32_e64 v125, -v127
	v_add_f32_e32 v112, 1.0, v112
	v_add_f32_e32 v113, 1.0, v113
	v_pk_mul_f32 v[110:111], v[110:111], v[180:181] op_sel_hi:[1,0]
	v_pk_mul_f32 v[106:107], v[106:107], v[114:115]
	v_rcp_f32_e32 v112, v112
	v_rcp_f32_e32 v113, v113
	v_exp_f32_e64 v114, -v110
	v_pk_mul_f32 v[100:101], v[100:101], v[182:183] op_sel_hi:[1,0]
	v_pk_mul_f32 v[118:119], v[126:127], v[118:119]
	v_add_f32_e32 v126, 1.0, v169
	v_add_f32_e32 v127, 1.0, v176
	v_pk_mul_f32 v[100:101], v[108:109], v[100:101]
	v_mov_b32_e32 v108, v171
	v_mov_b32_e32 v109, v172
	v_mov_b32_e32 v171, v173
	v_add_f32_e32 v169, 1.0, v124
	v_add_f32_e32 v176, 1.0, v125
	v_rcp_f32_e32 v124, v126
	v_rcp_f32_e32 v125, v127
	v_pk_add_f32 v[108:109], v[108:109], v[170:171]
	v_pk_mul_f32 v[100:101], v[100:101], v[112:113]
	v_add_f32_e32 v112, 1.0, v114
	v_add_f32_e32 v114, v108, v109
	v_add_f32_e32 v128, 1.0, v128
	v_add_f32_e32 v129, 1.0, v129
	v_add_f32_e32 v130, 1.0, v130
	v_add_f32_e32 v131, 1.0, v131
	ds_bpermute_b32 v115, v168, v114
	v_rcp_f32_e32 v126, v128
	v_rcp_f32_e32 v127, v129
	v_rcp_f32_e32 v128, v130
	v_rcp_f32_e32 v129, v131
	v_pk_mul_f32 v[120:121], v[120:121], v[124:125]
	v_exp_f32_e64 v113, -v111
	v_cvt_pk_fp8_f32 v174, v120, v121
	v_pk_mul_f32 v[116:117], v[116:117], v[128:129]
	v_rcp_f32_e32 v108, v112
	s_waitcnt lgkmcnt(0)
; __device__ __forceinline__ float rstd_fin4(const f32x4 a) { float s = (a[0] + a[1]) + (a[2] + a[3]); s += __shfl_xor(s, 16); s += __shfl_xor(s, 32); return __builtin_amdgcn_rsqf(s * (1.f / 1024.f) + 1e-6f); }
;     __device__ __forceinline__ void operator()(const f32x4 (&acc)[2][2][4][2], const Unit& u, int wr, int wc, int fr, int fq) const {
;     ...
;             for (int m = 0; m < 4; ++m) { const float rs = rstd_fin4(pa[ai][m]) * sc;
;                 const float rsl = rs * 1.4426950408889634f, rsu = rs * 0.6931471805599453f;
;                 f32x4 h0, h1;
; #pragma unroll
;                 for (int n = 0; n < 2; ++n) { const f32x4 G = acc[ai][0][m][n], U = acc[ai][1][m][n]; f32x4 hv;
; #pragma unroll
;                     for (int q = 0; q < 2; ++q) { const f32x2 g2 = (f32x2){G[2 * q], G[2 * q + 1]} * rsl, u2 = (f32x2){U[2 * q], U[2 * q + 1]} * rsu;
;                         f32x2 r2; r2.x = __builtin_amdgcn_rcpf(1.f + __builtin_amdgcn_exp2f(-g2.x)); r2.y = __builtin_amdgcn_rcpf(1.f + __builtin_amdgcn_exp2f(-g2.y));
;                         const f32x2 o2 = g2 * u2 * r2; hv[2 * q] = o2.x; hv[2 * q + 1] = o2.y; }
;                     if (n == 0) h0 = hv; else h1 = hv; }
;                 unsigned w0 = 0u, w1 = 0u;
;                 w0 = __builtin_amdgcn_cvt_pk_fp8_f32(h0[0], h0[1], w0, false); w0 = __builtin_amdgcn_cvt_pk_fp8_f32(h0[2], h0[3], w0, true); w1 = __builtin_amdgcn_cvt_pk_fp8_f32(h1[0], h1[1], w1, false); w1 = __builtin_amdgcn_cvt_pk_fp8_f32(h1[2], h1[3], w1, true);
;                 *(u32x2*)(hb + (ai * 4 + m) * 512) = (u32x2){w0, w1}; asm volatile("" ::: "memory"); }
	v_add_f32_e32 v112, v114, v115
	v_cvt_pk_fp8_f32 v175, v116, v117
	v_pk_mul_f32 v[116:117], v[122:123], v[126:127]
	v_add_f32_e32 v109, 1.0, v113
	ds_bpermute_b32 v113, v167, v112
	v_cvt_pk_fp8_f32 v174, v116, v117 op_sel:[0,0,1]
	v_add_f32_e32 v116, 1.0, v177
	v_add_f32_e32 v117, 1.0, v178
	v_rcp_f32_e32 v116, v116
	v_rcp_f32_e32 v117, v117
	v_pk_mul_f32 v[102:103], v[102:103], v[182:183] op_sel_hi:[1,0]
	v_rcp_f32_e32 v109, v109
	v_pk_mul_f32 v[102:103], v[110:111], v[102:103]
	v_mov_b32_e32 v111, v3
	v_cvt_pk_fp8_f32 v111, v100, v101
	s_waitcnt lgkmcnt(0)
	v_add_f32_e32 v100, v112, v113
	v_pk_mul_f32 v[104:105], v[104:105], v[116:117]
	v_mov_b32_e32 v110, v3
	v_fmamk_f32 v100, v100, 0x3a800000, v227
	v_cvt_pk_fp8_f32 v110, v104, v105
	v_rsq_f32_e32 v104, v100
	v_pk_mul_f32 v[100:101], v[102:103], v[108:109]
	v_rcp_f32_e32 v130, v169
	v_cvt_pk_fp8_f32 v111, v100, v101 op_sel:[0,0,1]
	v_mul_f32_e32 v100, 0x3fb8aa3b, v104
	v_pk_mul_f32 v[96:97], v[96:97], v[100:101] op_sel_hi:[1,0]
	v_mul_f32_e32 v102, 0x3f317218, v104
	v_exp_f32_e64 v101, -v96
	v_exp_f32_e64 v103, -v97
	v_rcp_f32_e32 v131, v176
	v_cvt_pk_fp8_f32 v110, v106, v107 op_sel:[0,0,1]
	v_add_f32_e32 v101, 1.0, v101
	v_pk_mul_f32 v[88:89], v[88:89], v[102:103] op_sel_hi:[1,0]
	v_rcp_f32_e32 v104, v101
	v_add_f32_e32 v101, 1.0, v103
	v_pk_mul_f32 v[88:89], v[96:97], v[88:89]
	v_pk_mul_f32 v[96:97], v[98:99], v[100:101] op_sel_hi:[1,0]
	v_pk_mul_f32 v[90:91], v[90:91], v[102:103] op_sel_hi:[1,0]
	v_pk_mul_f32 v[92:93], v[92:93], v[100:101] op_sel_hi:[1,0]
	v_exp_f32_e64 v98, -v96
	v_exp_f32_e64 v99, -v97
	v_pk_mul_f32 v[90:91], v[96:97], v[90:91]
	v_exp_f32_e64 v96, -v92
	v_exp_f32_e64 v97, -v93
	v_add_f32_e32 v98, 1.0, v98
	v_add_f32_e32 v99, 1.0, v99
	v_add_f32_e32 v96, 1.0, v96
	v_add_f32_e32 v97, 1.0, v97
	v_rcp_f32_e32 v96, v96
	v_rcp_f32_e32 v97, v97
	v_rcp_f32_e32 v98, v98
	v_rcp_f32_e32 v99, v99
	v_pk_mul_f32 v[84:85], v[84:85], v[102:103] op_sel_hi:[1,0]
	v_rcp_f32_e32 v105, v101
	v_pk_mul_f32 v[84:85], v[92:93], v[84:85]
	v_pk_mul_f32 v[90:91], v[90:91], v[98:99]
	v_pk_mul_f32 v[84:85], v[84:85], v[96:97]
	v_mov_b32_e32 v96, v149
	v_mov_b32_e32 v97, v150
	v_mov_b32_e32 v149, v151
	v_pk_add_f32 v[96:97], v[96:97], v[148:149]
	v_pk_mul_f32 v[92:93], v[94:95], v[100:101] op_sel_hi:[1,0]
	v_add_f32_e32 v98, v96, v97
	ds_bpermute_b32 v99, v168, v98
	v_exp_f32_e64 v94, -v92
	v_exp_f32_e64 v95, -v93
	v_pk_mul_f32 v[88:89], v[88:89], v[104:105]
	v_mov_b32_e32 v96, v3
	v_add_f32_e32 v94, 1.0, v94
	v_add_f32_e32 v95, 1.0, v95
	v_cvt_pk_fp8_f32 v96, v88, v89
	s_waitcnt lgkmcnt(0)
	v_add_f32_e32 v88, v98, v99
	v_rcp_f32_e32 v94, v94
	v_rcp_f32_e32 v95, v95
	v_mov_b32_e32 v97, v3
	ds_bpermute_b32 v89, v167, v88
	v_cvt_pk_fp8_f32 v97, v84, v85
	v_pk_mul_f32 v[86:87], v[86:87], v[102:103] op_sel_hi:[1,0]
	v_pk_mul_f32 v[118:119], v[118:119], v[130:131]
	v_pk_mul_f32 v[84:85], v[92:93], v[86:87]
	v_cvt_pk_fp8_f32 v175, v118, v119 op_sel:[0,0,1]
	v_pk_mul_f32 v[84:85], v[84:85], v[94:95]
	v_cvt_pk_fp8_f32 v96, v90, v91 op_sel:[0,0,1]
	v_cvt_pk_fp8_f32 v97, v84, v85 op_sel:[0,0,1]
	s_waitcnt lgkmcnt(0)
	v_add_f32_e32 v84, v88, v89
	v_fmamk_f32 v84, v84, 0x3a800000, v227
	v_rsq_f32_e32 v85, v84
	global_store_dwordx2 v[162:163], v[174:175], off nt
	global_store_dwordx2 v[162:163], v[110:111], off offset:512 nt
	v_mul_f32_e32 v84, 0x3fb8aa3b, v85
	v_pk_mul_f32 v[80:81], v[80:81], v[84:85] op_sel_hi:[1,0]
	v_mul_f32_e32 v86, 0x3f317218, v85
	v_exp_f32_e64 v87, -v80
	v_exp_f32_e64 v85, -v81
	global_store_dwordx2 v[162:163], v[96:97], off offset:1024 nt
	v_pk_mul_f32 v[72:73], v[72:73], v[86:87] op_sel_hi:[1,0]
	v_add_f32_e32 v87, 1.0, v87
	v_add_f32_e32 v85, 1.0, v85
	v_pk_mul_f32 v[72:73], v[80:81], v[72:73]
	v_pk_mul_f32 v[80:81], v[82:83], v[84:85] op_sel_hi:[1,0]
	v_pk_mul_f32 v[74:75], v[74:75], v[86:87] op_sel_hi:[1,0]
	v_pk_mul_f32 v[76:77], v[76:77], v[84:85] op_sel_hi:[1,0]
	v_exp_f32_e64 v82, -v80
	v_exp_f32_e64 v83, -v81
	v_pk_mul_f32 v[74:75], v[80:81], v[74:75]
	v_exp_f32_e64 v80, -v76
	v_exp_f32_e64 v81, -v77
	v_add_f32_e32 v82, 1.0, v82
	v_add_f32_e32 v83, 1.0, v83
	v_add_f32_e32 v80, 1.0, v80
	v_add_f32_e32 v81, 1.0, v81
	v_rcp_f32_e32 v80, v80
	v_rcp_f32_e32 v81, v81
	v_rcp_f32_e32 v82, v82
	v_rcp_f32_e32 v83, v83
	v_pk_mul_f32 v[68:69], v[68:69], v[86:87] op_sel_hi:[1,0]
	v_rcp_f32_e32 v88, v87
	v_pk_mul_f32 v[68:69], v[76:77], v[68:69]
	v_pk_mul_f32 v[74:75], v[74:75], v[82:83]
	v_pk_mul_f32 v[68:69], v[68:69], v[80:81]
	s_waitcnt vmcnt(6)
	v_mov_b32_e32 v80, v145
	v_mov_b32_e32 v81, v146
	v_mov_b32_e32 v145, v147
	v_pk_add_f32 v[80:81], v[80:81], v[144:145]
	v_rcp_f32_e32 v89, v85
	v_add_f32_e32 v82, v80, v81
	v_pk_mul_f32 v[76:77], v[78:79], v[84:85] op_sel_hi:[1,0]
	ds_bpermute_b32 v83, v168, v82
	v_exp_f32_e64 v78, -v76
	v_exp_f32_e64 v79, -v77
	v_pk_mul_f32 v[72:73], v[72:73], v[88:89]
	v_mov_b32_e32 v80, v3
	v_add_f32_e32 v78, 1.0, v78
	v_add_f32_e32 v79, 1.0, v79
	v_cvt_pk_fp8_f32 v80, v72, v73
	s_waitcnt lgkmcnt(0)
	v_add_f32_e32 v72, v82, v83
	v_rcp_f32_e32 v78, v78
	v_rcp_f32_e32 v79, v79
	v_mov_b32_e32 v81, v3
	ds_bpermute_b32 v73, v167, v72
	v_cvt_pk_fp8_f32 v81, v68, v69
	v_pk_mul_f32 v[70:71], v[70:71], v[86:87] op_sel_hi:[1,0]
	v_cvt_pk_fp8_f32 v80, v74, v75 op_sel:[0,0,1]
	v_pk_mul_f32 v[68:69], v[76:77], v[70:71]
	s_nop 0
	v_pk_mul_f32 v[68:69], v[68:69], v[78:79]
	s_nop 0
	v_cvt_pk_fp8_f32 v81, v68, v69 op_sel:[0,0,1]
	s_waitcnt lgkmcnt(0)
; __device__ __forceinline__ float rstd_fin4(const f32x4 a) { float s = (a[0] + a[1]) + (a[2] + a[3]); s += __shfl_xor(s, 16); s += __shfl_xor(s, 32); return __builtin_amdgcn_rsqf(s * (1.f / 1024.f) + 1e-6f); }
;     __device__ __forceinline__ void operator()(const f32x4 (&acc)[2][2][4][2], const Unit& u, int wr, int wc, int fr, int fq) const {
;     ...
;             for (int m = 0; m < 4; ++m) { const float rs = rstd_fin4(pa[ai][m]) * sc;
;                 const float rsl = rs * 1.4426950408889634f, rsu = rs * 0.6931471805599453f;
;                 f32x4 h0, h1;
; #pragma unroll
;                 for (int n = 0; n < 2; ++n) { const f32x4 G = acc[ai][0][m][n], U = acc[ai][1][m][n]; f32x4 hv;
; #pragma unroll
;                     for (int q = 0; q < 2; ++q) { const f32x2 g2 = (f32x2){G[2 * q], G[2 * q + 1]} * rsl, u2 = (f32x2){U[2 * q], U[2 * q + 1]} * rsu;
;                         f32x2 r2; r2.x = __builtin_amdgcn_rcpf(1.f + __builtin_amdgcn_exp2f(-g2.x)); r2.y = __builtin_amdgcn_rcpf(1.f + __builtin_amdgcn_exp2f(-g2.y));
;                         const f32x2 o2 = g2 * u2 * r2; hv[2 * q] = o2.x; hv[2 * q + 1] = o2.y; }
;                     if (n == 0) h0 = hv; else h1 = hv; }
;                 unsigned w0 = 0u, w1 = 0u;
;                 w0 = __builtin_amdgcn_cvt_pk_fp8_f32(h0[0], h0[1], w0, false); w0 = __builtin_amdgcn_cvt_pk_fp8_f32(h0[2], h0[3], w0, true); w1 = __builtin_amdgcn_cvt_pk_fp8_f32(h1[0], h1[1], w1, false); w1 = __builtin_amdgcn_cvt_pk_fp8_f32(h1[2], h1[3], w1, true);
;                 *(u32x2*)(hb + (ai * 4 + m) * 512) = (u32x2){w0, w1}; asm volatile("" ::: "memory"); }
	v_add_f32_e32 v68, v72, v73
	v_fmamk_f32 v68, v68, 0x3a800000, v227
	v_rsq_f32_e32 v69, v68
	global_store_dwordx2 v[162:163], v[80:81], off offset:1536 nt
	v_mul_f32_e32 v68, 0x3fb8aa3b, v69
	v_pk_mul_f32 v[64:65], v[64:65], v[68:69] op_sel_hi:[1,0]
	v_mul_f32_e32 v70, 0x3f317218, v69
	v_exp_f32_e64 v71, -v64
	v_exp_f32_e64 v69, -v65
	v_pk_mul_f32 v[56:57], v[56:57], v[70:71] op_sel_hi:[1,0]
	v_add_f32_e32 v69, 1.0, v69
	v_pk_mul_f32 v[56:57], v[64:65], v[56:57]
	v_pk_mul_f32 v[64:65], v[66:67], v[68:69] op_sel_hi:[1,0]
	v_add_f32_e32 v71, 1.0, v71
	v_exp_f32_e64 v66, -v64
	v_exp_f32_e64 v67, -v65
	v_pk_mul_f32 v[58:59], v[58:59], v[70:71] op_sel_hi:[1,0]
	v_pk_mul_f32 v[60:61], v[60:61], v[68:69] op_sel_hi:[1,0]
	v_add_f32_e32 v66, 1.0, v66
	v_add_f32_e32 v67, 1.0, v67
	v_pk_mul_f32 v[58:59], v[64:65], v[58:59]
	v_exp_f32_e64 v64, -v60
	v_exp_f32_e64 v65, -v61
	v_rcp_f32_e32 v66, v66
	v_rcp_f32_e32 v67, v67
	v_add_f32_e32 v64, 1.0, v64
	v_add_f32_e32 v65, 1.0, v65
	v_pk_mul_f32 v[62:63], v[62:63], v[68:69] op_sel_hi:[1,0]
	v_pk_mul_f32 v[58:59], v[58:59], v[66:67]
	v_rcp_f32_e32 v64, v64
	v_rcp_f32_e32 v65, v65
	v_exp_f32_e64 v66, -v62
	v_pk_mul_f32 v[52:53], v[52:53], v[70:71] op_sel_hi:[1,0]
	v_rcp_f32_e32 v72, v71
	v_pk_mul_f32 v[52:53], v[60:61], v[52:53]
	s_waitcnt vmcnt(6)
	v_mov_b32_e32 v60, v141
	v_mov_b32_e32 v61, v142
	v_mov_b32_e32 v141, v143
	v_pk_add_f32 v[60:61], v[60:61], v[140:141]
	v_pk_mul_f32 v[52:53], v[52:53], v[64:65]
	v_add_f32_e32 v64, 1.0, v66
	v_add_f32_e32 v66, v60, v61
	ds_bpermute_b32 v67, v168, v66
	v_exp_f32_e64 v65, -v63
	v_rcp_f32_e32 v60, v64
	v_rcp_f32_e32 v73, v69
	v_pk_mul_f32 v[54:55], v[54:55], v[70:71] op_sel_hi:[1,0]
	s_waitcnt lgkmcnt(0)
	v_add_f32_e32 v64, v66, v67
	v_add_f32_e32 v61, 1.0, v65
	ds_bpermute_b32 v65, v167, v64
	v_pk_mul_f32 v[54:55], v[62:63], v[54:55]
	v_mov_b32_e32 v63, v3
	v_cvt_pk_fp8_f32 v63, v52, v53
	v_pk_mul_f32 v[56:57], v[56:57], v[72:73]
	s_waitcnt lgkmcnt(0)
	v_add_f32_e32 v52, v64, v65
	v_rcp_f32_e32 v61, v61
	v_mov_b32_e32 v62, v3
	v_fmamk_f32 v52, v52, 0x3a800000, v227
	v_cvt_pk_fp8_f32 v62, v56, v57
	v_rsq_f32_e32 v56, v52
	v_pk_mul_f32 v[52:53], v[54:55], v[60:61]
	v_cvt_pk_fp8_f32 v62, v58, v59 op_sel:[0,0,1]
	v_cvt_pk_fp8_f32 v63, v52, v53 op_sel:[0,0,1]
	v_mul_f32_e32 v52, 0x3fb8aa3b, v56
	v_pk_mul_f32 v[48:49], v[48:49], v[52:53] op_sel_hi:[1,0]
	v_mul_f32_e32 v54, 0x3f317218, v56
	v_exp_f32_e64 v53, -v48
	v_exp_f32_e64 v55, -v49
	global_store_dwordx2 v[162:163], v[62:63], off offset:2048 nt
	v_add_f32_e32 v53, 1.0, v53
	v_pk_mul_f32 v[40:41], v[40:41], v[54:55] op_sel_hi:[1,0]
	v_rcp_f32_e32 v56, v53
	v_add_f32_e32 v53, 1.0, v55
	v_pk_mul_f32 v[40:41], v[48:49], v[40:41]
	v_pk_mul_f32 v[48:49], v[50:51], v[52:53] op_sel_hi:[1,0]
	v_pk_mul_f32 v[42:43], v[42:43], v[54:55] op_sel_hi:[1,0]
	v_pk_mul_f32 v[44:45], v[44:45], v[52:53] op_sel_hi:[1,0]
	v_exp_f32_e64 v50, -v48
	v_exp_f32_e64 v51, -v49
	v_pk_mul_f32 v[42:43], v[48:49], v[42:43]
	v_exp_f32_e64 v48, -v44
	v_exp_f32_e64 v49, -v45
	v_add_f32_e32 v50, 1.0, v50
	v_add_f32_e32 v51, 1.0, v51
	v_add_f32_e32 v48, 1.0, v48
	v_add_f32_e32 v49, 1.0, v49
	v_rcp_f32_e32 v48, v48
	v_rcp_f32_e32 v49, v49
	v_rcp_f32_e32 v50, v50
	v_rcp_f32_e32 v51, v51
	v_pk_mul_f32 v[36:37], v[36:37], v[54:55] op_sel_hi:[1,0]
	v_rcp_f32_e32 v57, v53
	v_pk_mul_f32 v[36:37], v[44:45], v[36:37]
	v_pk_mul_f32 v[42:43], v[42:43], v[50:51]
	v_pk_mul_f32 v[36:37], v[36:37], v[48:49]
	s_waitcnt vmcnt(6)
	v_mov_b32_e32 v48, v137
	v_mov_b32_e32 v49, v138
	v_mov_b32_e32 v137, v139
	v_pk_add_f32 v[48:49], v[48:49], v[136:137]
	v_pk_mul_f32 v[44:45], v[46:47], v[52:53] op_sel_hi:[1,0]
	v_add_f32_e32 v50, v48, v49
	ds_bpermute_b32 v51, v168, v50
	v_exp_f32_e64 v46, -v44
	v_exp_f32_e64 v47, -v45
	v_pk_mul_f32 v[40:41], v[40:41], v[56:57]
	v_mov_b32_e32 v48, v3
	v_add_f32_e32 v46, 1.0, v46
	v_add_f32_e32 v47, 1.0, v47
	v_cvt_pk_fp8_f32 v48, v40, v41
	s_waitcnt lgkmcnt(0)
	v_add_f32_e32 v40, v50, v51
	v_rcp_f32_e32 v46, v46
	v_rcp_f32_e32 v47, v47
	v_mov_b32_e32 v49, v3
	ds_bpermute_b32 v41, v167, v40
	v_cvt_pk_fp8_f32 v49, v36, v37
	v_pk_mul_f32 v[38:39], v[38:39], v[54:55] op_sel_hi:[1,0]
	v_cvt_pk_fp8_f32 v48, v42, v43 op_sel:[0,0,1]
	v_pk_mul_f32 v[36:37], v[44:45], v[38:39]
	s_nop 0
	v_pk_mul_f32 v[36:37], v[36:37], v[46:47]
	s_nop 0
	v_cvt_pk_fp8_f32 v49, v36, v37 op_sel:[0,0,1]
	s_waitcnt lgkmcnt(0)
; __device__ __forceinline__ float rstd_fin4(const f32x4 a) { float s = (a[0] + a[1]) + (a[2] + a[3]); s += __shfl_xor(s, 16); s += __shfl_xor(s, 32); return __builtin_amdgcn_rsqf(s * (1.f / 1024.f) + 1e-6f); }
;     __device__ __forceinline__ void operator()(const f32x4 (&acc)[2][2][4][2], const Unit& u, int wr, int wc, int fr, int fq) const {
;     ...
;             for (int m = 0; m < 4; ++m) { const float rs = rstd_fin4(pa[ai][m]) * sc;
;                 const float rsl = rs * 1.4426950408889634f, rsu = rs * 0.6931471805599453f;
;                 f32x4 h0, h1;
; #pragma unroll
;                 for (int n = 0; n < 2; ++n) { const f32x4 G = acc[ai][0][m][n], U = acc[ai][1][m][n]; f32x4 hv;
; #pragma unroll
;                     for (int q = 0; q < 2; ++q) { const f32x2 g2 = (f32x2){G[2 * q], G[2 * q + 1]} * rsl, u2 = (f32x2){U[2 * q], U[2 * q + 1]} * rsu;
;                         f32x2 r2; r2.x = __builtin_amdgcn_rcpf(1.f + __builtin_amdgcn_exp2f(-g2.x)); r2.y = __builtin_amdgcn_rcpf(1.f + __builtin_amdgcn_exp2f(-g2.y));
;                         const f32x2 o2 = g2 * u2 * r2; hv[2 * q] = o2.x; hv[2 * q + 1] = o2.y; }
;                     if (n == 0) h0 = hv; else h1 = hv; }
;                 unsigned w0 = 0u, w1 = 0u;
;                 w0 = __builtin_amdgcn_cvt_pk_fp8_f32(h0[0], h0[1], w0, false); w0 = __builtin_amdgcn_cvt_pk_fp8_f32(h0[2], h0[3], w0, true); w1 = __builtin_amdgcn_cvt_pk_fp8_f32(h1[0], h1[1], w1, false); w1 = __builtin_amdgcn_cvt_pk_fp8_f32(h1[2], h1[3], w1, true);
;                 *(u32x2*)(hb + (ai * 4 + m) * 512) = (u32x2){w0, w1}; asm volatile("" ::: "memory"); }
	v_add_f32_e32 v36, v40, v41
	v_fmamk_f32 v36, v36, 0x3a800000, v227
	v_rsq_f32_e32 v37, v36
	global_store_dwordx2 v[162:163], v[48:49], off offset:2560 nt
	v_mul_f32_e32 v36, 0x3fb8aa3b, v37
	v_pk_mul_f32 v[32:33], v[32:33], v[36:37] op_sel_hi:[1,0]
	v_mul_f32_e32 v38, 0x3f317218, v37
	v_exp_f32_e64 v39, -v32
	v_exp_f32_e64 v37, -v33
	v_pk_mul_f32 v[24:25], v[24:25], v[38:39] op_sel_hi:[1,0]
	v_add_f32_e32 v37, 1.0, v37
	v_pk_mul_f32 v[24:25], v[32:33], v[24:25]
	v_pk_mul_f32 v[32:33], v[34:35], v[36:37] op_sel_hi:[1,0]
	v_add_f32_e32 v39, 1.0, v39
	v_exp_f32_e64 v34, -v32
	v_exp_f32_e64 v35, -v33
	v_pk_mul_f32 v[26:27], v[26:27], v[38:39] op_sel_hi:[1,0]
	v_pk_mul_f32 v[28:29], v[28:29], v[36:37] op_sel_hi:[1,0]
	v_add_f32_e32 v34, 1.0, v34
	v_add_f32_e32 v35, 1.0, v35
	v_pk_mul_f32 v[26:27], v[32:33], v[26:27]
	v_exp_f32_e64 v32, -v28
	v_exp_f32_e64 v33, -v29
	v_rcp_f32_e32 v34, v34
	v_rcp_f32_e32 v35, v35
	v_add_f32_e32 v32, 1.0, v32
	v_add_f32_e32 v33, 1.0, v33
	v_pk_mul_f32 v[30:31], v[30:31], v[36:37] op_sel_hi:[1,0]
	v_pk_mul_f32 v[26:27], v[26:27], v[34:35]
	v_rcp_f32_e32 v32, v32
	v_rcp_f32_e32 v33, v33
	v_exp_f32_e64 v34, -v30
	v_pk_mul_f32 v[20:21], v[20:21], v[38:39] op_sel_hi:[1,0]
	v_rcp_f32_e32 v40, v39
	v_pk_mul_f32 v[20:21], v[28:29], v[20:21]
	s_waitcnt vmcnt(6)
	v_mov_b32_e32 v28, v133
	v_mov_b32_e32 v29, v134
	v_mov_b32_e32 v133, v135
	v_pk_add_f32 v[28:29], v[28:29], v[132:133]
	v_pk_mul_f32 v[20:21], v[20:21], v[32:33]
	v_add_f32_e32 v32, 1.0, v34
	v_add_f32_e32 v34, v28, v29
	ds_bpermute_b32 v35, v168, v34
	v_exp_f32_e64 v33, -v31
	v_rcp_f32_e32 v28, v32
	v_rcp_f32_e32 v41, v37
	v_pk_mul_f32 v[22:23], v[22:23], v[38:39] op_sel_hi:[1,0]
	s_waitcnt lgkmcnt(0)
	v_add_f32_e32 v32, v34, v35
	v_add_f32_e32 v29, 1.0, v33
	ds_bpermute_b32 v33, v167, v32
	v_pk_mul_f32 v[22:23], v[30:31], v[22:23]
	v_mov_b32_e32 v31, v3
	v_cvt_pk_fp8_f32 v31, v20, v21
	v_pk_mul_f32 v[24:25], v[24:25], v[40:41]
	s_waitcnt lgkmcnt(0)
	v_add_f32_e32 v20, v32, v33
	v_rcp_f32_e32 v29, v29
	v_mov_b32_e32 v30, v3
	v_fmamk_f32 v20, v20, 0x3a800000, v227
	v_cvt_pk_fp8_f32 v30, v24, v25
	v_rsq_f32_e32 v24, v20
	v_pk_mul_f32 v[20:21], v[22:23], v[28:29]
	v_cvt_pk_fp8_f32 v30, v26, v27 op_sel:[0,0,1]
	v_cvt_pk_fp8_f32 v31, v20, v21 op_sel:[0,0,1]
	v_mul_f32_e32 v20, 0x3fb8aa3b, v24
	v_pk_mul_f32 v[16:17], v[16:17], v[20:21] op_sel_hi:[1,0]
	v_mul_f32_e32 v22, 0x3f317218, v24
	v_exp_f32_e64 v21, -v16
	v_exp_f32_e64 v23, -v17
	global_store_dwordx2 v[162:163], v[30:31], off offset:3072 nt
	v_add_f32_e32 v21, 1.0, v21
	v_pk_mul_f32 v[8:9], v[8:9], v[22:23] op_sel_hi:[1,0]
	v_rcp_f32_e32 v24, v21
	v_add_f32_e32 v21, 1.0, v23
	v_pk_mul_f32 v[8:9], v[16:17], v[8:9]
	v_pk_mul_f32 v[16:17], v[18:19], v[20:21] op_sel_hi:[1,0]
	v_pk_mul_f32 v[10:11], v[10:11], v[22:23] op_sel_hi:[1,0]
	v_pk_mul_f32 v[12:13], v[12:13], v[20:21] op_sel_hi:[1,0]
	v_exp_f32_e64 v18, -v16
	v_exp_f32_e64 v19, -v17
	v_pk_mul_f32 v[10:11], v[16:17], v[10:11]
	v_exp_f32_e64 v16, -v12
	v_exp_f32_e64 v17, -v13
	v_pk_mul_f32 v[4:5], v[4:5], v[22:23] op_sel_hi:[1,0]
	v_rcp_f32_e32 v25, v21
	v_pk_mul_f32 v[4:5], v[12:13], v[4:5]
	v_pk_mul_f32 v[12:13], v[14:15], v[20:21] op_sel_hi:[1,0]
	v_add_f32_e32 v16, 1.0, v16
	v_add_f32_e32 v17, 1.0, v17
	v_exp_f32_e64 v14, -v12
	v_exp_f32_e64 v15, -v13
	v_rcp_f32_e32 v16, v16
	v_rcp_f32_e32 v17, v17
	v_add_f32_e32 v18, 1.0, v18
	v_add_f32_e32 v19, 1.0, v19
	v_add_f32_e32 v14, 1.0, v14
	v_add_f32_e32 v15, 1.0, v15
	v_pk_mul_f32 v[8:9], v[8:9], v[24:25]
	v_rcp_f32_e32 v18, v18
	v_rcp_f32_e32 v19, v19
	v_pk_mul_f32 v[4:5], v[4:5], v[16:17]
	v_rcp_f32_e32 v14, v14
	v_rcp_f32_e32 v15, v15
	v_mov_b32_e32 v16, v3
	v_mov_b32_e32 v17, v3
	v_cvt_pk_fp8_f32 v16, v8, v9
	v_cvt_pk_fp8_f32 v17, v4, v5
	v_pk_mul_f32 v[6:7], v[6:7], v[22:23] op_sel_hi:[1,0]
	v_pk_mul_f32 v[10:11], v[10:11], v[18:19]
	v_pk_mul_f32 v[4:5], v[12:13], v[6:7]
	v_cvt_pk_fp8_f32 v16, v10, v11 op_sel:[0,0,1]
	v_pk_mul_f32 v[4:5], v[4:5], v[14:15]
	s_nop 0
	v_cvt_pk_fp8_f32 v17, v4, v5 op_sel:[0,0,1]
	global_store_dwordx2 v[162:163], v[16:17], off offset:3584 nt
	s_cbranch_vccnz .LBB0_427
	s_andn2_b64 vcc, exec, s[44:45]
	s_cbranch_vccnz .LBB0_426
	s_barrier
	s_branch .LBB0_426

; __device__ __forceinline__ float rstd_fin4(const f32x4 a) { float s = (a[0] + a[1]) + (a[2] + a[3]); s += __shfl_xor(s, 16); s += __shfl_xor(s, 32); return __builtin_amdgcn_rsqf(s * (1.f / 1024.f) + 1e-6f); }
;     __device__ __forceinline__ void operator()(const f32x4 (&acc)[2][2][4][2], const Unit& u, int wr, int wc, int fr, int fq) const {
;     ...
;         const int row0 = u.pm * BM + wr * 64 + fr;
;         unsigned char* const hb = (unsigned char*)H + (size_t)(u.pm * (FFH / 128) + u.pn + pn0) * 32768 + (((wr * 4 + wc) * 8) * 64 + (fq >> 1) * 32 + fr * 2 + (fq & 1)) * 8;
;         f32x4 pa[2][4];
; #pragma unroll
;         for (int ai = 0; ai < 2; ++ai)
; #pragma unroll
;             for (int m = 0; m < 4; ++m) pa[ai][m] = rstd_ld4(ss, row0 + ai * HALF + m * 16, fq);
; #pragma unroll
;         for (int ai = 0; ai < 2; ++ai)
; #pragma unroll
;             for (int m = 0; m < 4; ++m) { const float rs = rstd_fin4(pa[ai][m]) * sc;
;                 const float rsl = rs * 1.4426950408889634f, rsu = rs * 0.6931471805599453f;
;                 f32x4 h0, h1;
; #pragma unroll
;                 for (int n = 0; n < 2; ++n) { const f32x4 G = acc[ai][0][m][n], U = acc[ai][1][m][n]; f32x4 hv;
; #pragma unroll
;                     for (int q = 0; q < 2; ++q) { const f32x2 g2 = (f32x2){G[2 * q], G[2 * q + 1]} * rsl, u2 = (f32x2){U[2 * q], U[2 * q + 1]} * rsu;
;                         f32x2 r2; r2.x = __builtin_amdgcn_rcpf(1.f + __builtin_amdgcn_exp2f(-g2.x)); r2.y = __builtin_amdgcn_rcpf(1.f + __builtin_amdgcn_exp2f(-g2.y));
.LBB0_1674:
	s_lshl_b32 s4, s72, 8
	v_mov_b32_e32 v14, v1
	v_mov_b32_e32 v15, v182
	s_add_i32 s4, s4, s66
	v_and_b32_e32 v17, 64, v246
	v_add_u32_e32 v4, s4, v14
	v_lshlrev_b32_e32 v6, 2, v15
	v_ashrrev_i32_e32 v7, 31, v6
	v_ashrrev_i32_e32 v5, 31, v4
	v_lshl_add_u64 v[6:7], v[6:7], 2, s[44:45]
	v_lshlrev_b64 v[4:5], 6, v[4:5]
	v_lshl_add_u64 v[12:13], v[6:7], 0, v[4:5]
	global_load_dwordx4 v[4:7], v[12:13], off
	global_load_dwordx4 v[8:11], v[12:13], off offset:1024
	global_load_dwordx4 v[28:31], v[12:13], off offset:2048
	global_load_dwordx4 v[20:23], v[12:13], off offset:3072
	v_xor_b32_e32 v16, 16, v246
	v_add_u32_e32 v17, 64, v17
	v_xor_b32_e32 v18, 32, v246
	v_cmp_lt_i32_e32 vcc, v16, v17
	v_mov_b32_e32 v32, v3
	v_mov_b32_e32 v33, v3
	v_cndmask_b32_e32 v16, v246, v16, vcc
	v_cmp_lt_i32_e32 vcc, v18, v17
	v_lshlrev_b32_e32 v27, 2, v16
	s_mul_i32 s4, s72, 22
	v_cndmask_b32_e32 v17, v246, v18, vcc
	v_lshlrev_b32_e32 v26, 2, v17
	s_add_i32 s4, s4, s71
	s_ashr_i32 s5, s4, 31
	v_lshlrev_b32_e32 v19, 4, v15
	v_lshl_add_u32 v14, v14, 1, s69
	s_lshl_b64 s[4:5], s[4:5], 15
	v_and_b32_e32 v18, 0x1fffffe0, v19
	v_and_or_b32 v14, v15, 1, v14
	v_add_lshl_u32 v14, v14, v18, 3
	s_add_u32 s4, s6, s4
	v_ashrrev_i32_e32 v15, 31, v14
	s_addc_u32 s5, s7, s5
	v_lshl_add_u64 v[24:25], s[4:5], 0, v[14:15]
	s_mov_b64 s[4:5], -1
	s_waitcnt vmcnt(0)
	v_mov_b32_e32 v16, v5
	v_mov_b32_e32 v17, v6
	v_mov_b32_e32 v5, v7
	v_mov_b32_e32 v6, v9
	v_mov_b32_e32 v7, v10
	v_mov_b32_e32 v9, v11
	v_pk_add_f32 v[4:5], v[16:17], v[4:5]
	v_pk_add_f32 v[6:7], v[6:7], v[8:9]
	v_add_f32_e32 v8, v4, v5
	v_add_f32_e32 v6, v6, v7
	ds_bpermute_b32 v7, v27, v8
	ds_bpermute_b32 v9, v27, v6
	v_add_co_u32_e32 v4, vcc, s88, v12
	s_waitcnt lgkmcnt(1)
	v_add_f32_e32 v7, v8, v7
	s_waitcnt lgkmcnt(0)
	v_add_f32_e32 v6, v6, v9
	ds_bpermute_b32 v8, v26, v7
	ds_bpermute_b32 v9, v26, v6
	v_addc_co_u32_e32 v5, vcc, 0, v13, vcc
	global_load_dwordx4 v[16:19], v[4:5], off
	global_load_dwordx4 v[12:15], v[4:5], off offset:1024
	s_waitcnt lgkmcnt(1)
	v_add_f32_e32 v7, v7, v8
	s_waitcnt lgkmcnt(0)
	v_add_f32_e32 v6, v6, v9
	v_fmamk_f32 v7, v7, 0x3a800000, v227
	v_fmamk_f32 v6, v6, 0x3a800000, v227
	v_rsq_f32_e32 v34, v7
	v_rsq_f32_e32 v35, v6
	global_load_dwordx4 v[8:11], v[4:5], off offset:2048
	s_nop 0
	global_load_dwordx4 v[4:7], v[4:5], off offset:3072
	s_andn2_b64 vcc, exec, s[40:41]
	v_mul_f32_e32 v174, 0x3c800000, v34
	v_mul_f32_e32 v35, 0x3c800000, v35
	v_mul_f32_e32 v34, 0x3fb8aa3b, v174
	v_mul_f32_e32 v174, 0x3f317218, v174
	v_pk_mul_f32 v[160:161], v[160:161], v[34:35] op_sel_hi:[1,0]
	v_pk_mul_f32 v[152:153], v[152:153], v[174:175] op_sel_hi:[1,0]
	v_pk_mul_f32 v[162:163], v[162:163], v[34:35] op_sel_hi:[1,0]
	v_pk_mul_f32 v[154:155], v[154:155], v[174:175] op_sel_hi:[1,0]
	v_pk_mul_f32 v[156:157], v[156:157], v[34:35] op_sel_hi:[1,0]
	v_mul_f32_e32 v176, 0x3fb8aa3b, v35
	v_mul_f32_e32 v178, 0x3f317218, v35
	v_pk_mul_f32 v[148:149], v[148:149], v[174:175] op_sel_hi:[1,0]
	v_pk_mul_f32 v[34:35], v[158:159], v[34:35] op_sel_hi:[1,0]
	v_exp_f32_e64 v158, -v160
	v_exp_f32_e64 v159, -v161
	v_pk_mul_f32 v[152:153], v[160:161], v[152:153]
	v_exp_f32_e64 v160, -v162
	v_exp_f32_e64 v161, -v163
	v_pk_mul_f32 v[154:155], v[162:163], v[154:155]
	v_exp_f32_e64 v162, -v156
	v_exp_f32_e64 v163, -v157
	v_pk_mul_f32 v[148:149], v[156:157], v[148:149]
	v_exp_f32_e64 v156, -v34
	v_exp_f32_e64 v157, -v35
	v_pk_mul_f32 v[150:151], v[150:151], v[174:175] op_sel_hi:[1,0]
	v_pk_mul_f32 v[144:145], v[144:145], v[176:177] op_sel_hi:[1,0]
	v_pk_mul_f32 v[34:35], v[34:35], v[150:151]
	v_add_f32_e32 v150, 1.0, v158
	v_add_f32_e32 v151, 1.0, v159
	v_add_f32_e32 v158, 1.0, v160
	v_add_f32_e32 v159, 1.0, v161
	v_add_f32_e32 v160, 1.0, v162
	v_add_f32_e32 v161, 1.0, v163
	v_add_f32_e32 v162, 1.0, v156
	v_add_f32_e32 v163, 1.0, v157
	v_rcp_f32_e32 v150, v150
	v_rcp_f32_e32 v151, v151
	v_rcp_f32_e32 v156, v158
	v_rcp_f32_e32 v157, v159
	v_rcp_f32_e32 v158, v160
	v_rcp_f32_e32 v159, v161
	v_rcp_f32_e32 v160, v162
	v_rcp_f32_e32 v161, v163
	v_pk_mul_f32 v[150:151], v[152:153], v[150:151]
	v_pk_mul_f32 v[148:149], v[148:149], v[158:159]
	v_cvt_pk_fp8_f32 v32, v150, v151
	v_cvt_pk_fp8_f32 v33, v148, v149
	v_pk_mul_f32 v[148:149], v[154:155], v[156:157]
	v_pk_mul_f32 v[34:35], v[34:35], v[160:161]
	v_cvt_pk_fp8_f32 v32, v148, v149 op_sel:[0,0,1]
	v_cvt_pk_fp8_f32 v33, v34, v35 op_sel:[0,0,1]
	v_exp_f32_e64 v35, -v145
	v_exp_f32_e64 v174, -v144
	v_pk_mul_f32 v[136:137], v[136:137], v[178:179] op_sel_hi:[1,0]
	global_store_dwordx2 v[24:25], v[32:33], off nt
	v_add_f32_e32 v32, 1.0, v35
	v_add_f32_e32 v34, 1.0, v174
	v_rcp_f32_e32 v35, v32
	v_pk_mul_f32 v[32:33], v[144:145], v[136:137]
	v_pk_mul_f32 v[136:137], v[146:147], v[176:177] op_sel_hi:[1,0]
	v_rcp_f32_e32 v34, v34
	v_exp_f32_e64 v144, -v136
	v_exp_f32_e64 v145, -v137
	v_pk_mul_f32 v[132:133], v[132:133], v[178:179] op_sel_hi:[1,0]
	v_pk_mul_f32 v[32:33], v[32:33], v[34:35]
	v_pk_mul_f32 v[34:35], v[138:139], v[178:179] op_sel_hi:[1,0]
	v_add_f32_e32 v138, 1.0, v144
	v_add_f32_e32 v139, 1.0, v145
	v_rcp_f32_e32 v138, v138
	v_rcp_f32_e32 v139, v139
	v_pk_mul_f32 v[34:35], v[136:137], v[34:35]
	v_pk_mul_f32 v[136:137], v[140:141], v[176:177] op_sel_hi:[1,0]
	v_pk_mul_f32 v[134:135], v[134:135], v[178:179] op_sel_hi:[1,0]
	v_exp_f32_e64 v140, -v136
	v_pk_mul_f32 v[34:35], v[34:35], v[138:139]
	v_exp_f32_e64 v139, -v137
	v_pk_mul_f32 v[132:133], v[136:137], v[132:133]
	v_mov_b32_e32 v136, v29
	v_mov_b32_e32 v137, v30
	v_mov_b32_e32 v29, v31
	v_pk_add_f32 v[28:29], v[136:137], v[28:29]
	v_add_f32_e32 v138, 1.0, v140
	v_add_f32_e32 v136, v28, v29
	ds_bpermute_b32 v137, v27, v136
	v_add_f32_e32 v139, 1.0, v139
	v_rcp_f32_e32 v138, v138
	v_rcp_f32_e32 v139, v139
	v_pk_mul_f32 v[140:141], v[142:143], v[176:177] op_sel_hi:[1,0]
	s_waitcnt lgkmcnt(0)
; __device__ __forceinline__ float rstd_fin4(const f32x4 a) { float s = (a[0] + a[1]) + (a[2] + a[3]); s += __shfl_xor(s, 16); s += __shfl_xor(s, 32); return __builtin_amdgcn_rsqf(s * (1.f / 1024.f) + 1e-6f); }
;     __device__ __forceinline__ void operator()(const f32x4 (&acc)[2][2][4][2], const Unit& u, int wr, int wc, int fr, int fq) const {
;     ...
;             for (int m = 0; m < 4; ++m) { const float rs = rstd_fin4(pa[ai][m]) * sc;
;                 const float rsl = rs * 1.4426950408889634f, rsu = rs * 0.6931471805599453f;
;                 f32x4 h0, h1;
; #pragma unroll
;                 for (int n = 0; n < 2; ++n) { const f32x4 G = acc[ai][0][m][n], U = acc[ai][1][m][n]; f32x4 hv;
; #pragma unroll
;                     for (int q = 0; q < 2; ++q) { const f32x2 g2 = (f32x2){G[2 * q], G[2 * q + 1]} * rsl, u2 = (f32x2){U[2 * q], U[2 * q + 1]} * rsu;
;                         f32x2 r2; r2.x = __builtin_amdgcn_rcpf(1.f + __builtin_amdgcn_exp2f(-g2.x)); r2.y = __builtin_amdgcn_rcpf(1.f + __builtin_amdgcn_exp2f(-g2.y));
;                         const f32x2 o2 = g2 * u2 * r2; hv[2 * q] = o2.x; hv[2 * q + 1] = o2.y; }
;                     if (n == 0) h0 = hv; else h1 = hv; }
;                 unsigned w0 = 0u, w1 = 0u;
;                 w0 = __builtin_amdgcn_cvt_pk_fp8_f32(h0[0], h0[1], w0, false); w0 = __builtin_amdgcn_cvt_pk_fp8_f32(h0[2], h0[3], w0, true); w1 = __builtin_amdgcn_cvt_pk_fp8_f32(h1[0], h1[1], w1, false); w1 = __builtin_amdgcn_cvt_pk_fp8_f32(h1[2], h1[3], w1, true);
;                 *(u32x2*)(hb + (ai * 4 + m) * 512) = (u32x2){w0, w1}; asm volatile("" ::: "memory"); }
	v_add_f32_e32 v136, v136, v137
	ds_bpermute_b32 v137, v26, v136
	v_exp_f32_e64 v142, -v140
	v_pk_mul_f32 v[132:133], v[132:133], v[138:139]
	v_exp_f32_e64 v139, -v141
	v_pk_mul_f32 v[30:31], v[140:141], v[134:135]
	v_mov_b32_e32 v134, v3
	v_add_f32_e32 v138, 1.0, v142
	v_add_f32_e32 v29, 1.0, v139
	v_cvt_pk_fp8_f32 v134, v32, v33
	s_waitcnt lgkmcnt(0)
	v_add_f32_e32 v32, v136, v137
	v_rcp_f32_e32 v28, v138
	v_rcp_f32_e32 v29, v29
	v_mov_b32_e32 v135, v3
	v_fmamk_f32 v32, v32, 0x3a800000, v227
	v_cvt_pk_fp8_f32 v135, v132, v133
	v_rsq_f32_e32 v32, v32
	v_pk_mul_f32 v[28:29], v[30:31], v[28:29]
	v_cvt_pk_fp8_f32 v134, v34, v35 op_sel:[0,0,1]
	v_cvt_pk_fp8_f32 v135, v28, v29 op_sel:[0,0,1]
	v_mul_f32_e32 v29, 0x3c800000, v32
	v_mul_f32_e32 v28, 0x3fb8aa3b, v29
	v_pk_mul_f32 v[30:31], v[128:129], v[28:29] op_sel_hi:[1,0]
	v_mul_f32_e32 v32, 0x3f317218, v29
	v_exp_f32_e64 v33, -v30
	v_exp_f32_e64 v29, -v31
	global_store_dwordx2 v[24:25], v[134:135], off offset:512 nt
	v_pk_mul_f32 v[34:35], v[120:121], v[32:33] op_sel_hi:[1,0]
	v_add_f32_e32 v29, 1.0, v29
	v_pk_mul_f32 v[30:31], v[30:31], v[34:35]
	v_pk_mul_f32 v[34:35], v[130:131], v[28:29] op_sel_hi:[1,0]
	v_add_f32_e32 v33, 1.0, v33
	v_rcp_f32_e32 v121, v29
	v_exp_f32_e64 v29, -v34
	v_rcp_f32_e32 v120, v33
	v_exp_f32_e64 v33, -v35
	v_add_f32_e32 v29, 1.0, v29
	v_pk_mul_f32 v[30:31], v[30:31], v[120:121]
	v_pk_mul_f32 v[120:121], v[122:123], v[32:33] op_sel_hi:[1,0]
	v_rcp_f32_e32 v122, v29
	v_add_f32_e32 v29, 1.0, v33
	v_pk_mul_f32 v[34:35], v[34:35], v[120:121]
	v_pk_mul_f32 v[120:121], v[124:125], v[28:29] op_sel_hi:[1,0]
	v_rcp_f32_e32 v123, v29
	v_exp_f32_e64 v29, -v120
	v_exp_f32_e64 v33, -v121
	v_pk_mul_f32 v[34:35], v[34:35], v[122:123]
	v_add_f32_e32 v29, 1.0, v29
	v_rcp_f32_e32 v122, v29
	v_add_f32_e32 v29, 1.0, v33
	v_pk_mul_f32 v[116:117], v[116:117], v[32:33] op_sel_hi:[1,0]
	v_rcp_f32_e32 v123, v29
	v_pk_mul_f32 v[28:29], v[126:127], v[28:29] op_sel_hi:[1,0]
	v_pk_mul_f32 v[116:117], v[120:121], v[116:117]
	v_exp_f32_e64 v120, -v28
	v_exp_f32_e64 v121, -v29
	v_pk_mul_f32 v[32:33], v[118:119], v[32:33] op_sel_hi:[1,0]
	v_pk_mul_f32 v[116:117], v[116:117], v[122:123]
	v_add_f32_e32 v118, 1.0, v120
	v_add_f32_e32 v119, 1.0, v121
	v_mov_b32_e32 v120, v21
	v_mov_b32_e32 v121, v22
	v_mov_b32_e32 v21, v23
	v_pk_add_f32 v[20:21], v[120:121], v[20:21]
	v_rcp_f32_e32 v118, v118
	v_add_f32_e32 v22, v20, v21
	ds_bpermute_b32 v23, v27, v22
	v_mov_b32_e32 v20, v3
	v_cvt_pk_fp8_f32 v20, v30, v31
	v_rcp_f32_e32 v119, v119
	v_mov_b32_e32 v21, v3
	s_waitcnt lgkmcnt(0)
	v_add_f32_e32 v30, v22, v23
	ds_bpermute_b32 v31, v26, v30
	v_cvt_pk_fp8_f32 v21, v116, v117
	v_pk_mul_f32 v[22:23], v[28:29], v[32:33]
	v_cvt_pk_fp8_f32 v20, v34, v35 op_sel:[0,0,1]
	v_pk_mul_f32 v[22:23], v[22:23], v[118:119]
	s_nop 0
	v_cvt_pk_fp8_f32 v21, v22, v23 op_sel:[0,0,1]
	s_waitcnt lgkmcnt(0)
	v_add_f32_e32 v22, v30, v31
	v_fmamk_f32 v22, v22, 0x3a800000, v227
	v_rsq_f32_e32 v22, v22
	global_store_dwordx2 v[24:25], v[20:21], off offset:1024 nt
	v_mul_f32_e32 v21, 0x3c800000, v22
	v_mul_f32_e32 v20, 0x3fb8aa3b, v21
	v_pk_mul_f32 v[22:23], v[112:113], v[20:21] op_sel_hi:[1,0]
	v_mul_f32_e32 v28, 0x3f317218, v21
	v_exp_f32_e64 v29, -v22
	v_exp_f32_e64 v21, -v23
	v_pk_mul_f32 v[30:31], v[104:105], v[28:29] op_sel_hi:[1,0]
	v_add_f32_e32 v21, 1.0, v21
	v_pk_mul_f32 v[22:23], v[22:23], v[30:31]
	v_pk_mul_f32 v[30:31], v[114:115], v[20:21] op_sel_hi:[1,0]
	v_add_f32_e32 v29, 1.0, v29
	v_rcp_f32_e32 v33, v21
	v_exp_f32_e64 v21, -v30
	v_rcp_f32_e32 v32, v29
	v_exp_f32_e64 v29, -v31
	v_add_f32_e32 v21, 1.0, v21
	v_pk_mul_f32 v[22:23], v[22:23], v[32:33]
	v_pk_mul_f32 v[32:33], v[106:107], v[28:29] op_sel_hi:[1,0]
	v_rcp_f32_e32 v34, v21
	v_add_f32_e32 v21, 1.0, v29
	v_pk_mul_f32 v[30:31], v[30:31], v[32:33]
	v_pk_mul_f32 v[32:33], v[108:109], v[20:21] op_sel_hi:[1,0]
	v_rcp_f32_e32 v35, v21
	v_exp_f32_e64 v21, -v32
	v_exp_f32_e64 v29, -v33
	v_pk_mul_f32 v[30:31], v[30:31], v[34:35]
	v_add_f32_e32 v21, 1.0, v21
	v_pk_mul_f32 v[34:35], v[100:101], v[28:29] op_sel_hi:[1,0]
	v_rcp_f32_e32 v100, v21
	v_add_f32_e32 v21, 1.0, v29
	v_rcp_f32_e32 v101, v21
	v_pk_mul_f32 v[32:33], v[32:33], v[34:35]
	v_pk_mul_f32 v[20:21], v[110:111], v[20:21] op_sel_hi:[1,0]
	v_pk_mul_f32 v[28:29], v[102:103], v[28:29] op_sel_hi:[1,0]
	v_pk_mul_f32 v[32:33], v[32:33], v[100:101]
	s_waitcnt vmcnt(6)
	v_mov_b32_e32 v100, v17
	v_mov_b32_e32 v101, v18
	v_mov_b32_e32 v17, v19
	v_pk_add_f32 v[16:17], v[100:101], v[16:17]
	v_exp_f32_e64 v34, -v20
	v_add_f32_e32 v18, v16, v17
	ds_bpermute_b32 v19, v27, v18
	v_exp_f32_e64 v35, -v21
	v_mov_b32_e32 v16, v3
	v_add_f32_e32 v34, 1.0, v34
	v_cvt_pk_fp8_f32 v16, v22, v23
	v_add_f32_e32 v35, 1.0, v35
	s_waitcnt lgkmcnt(0)
	v_add_f32_e32 v22, v18, v19
	v_rcp_f32_e32 v34, v34
	v_rcp_f32_e32 v35, v35
	v_mov_b32_e32 v17, v3
	ds_bpermute_b32 v23, v26, v22
	v_cvt_pk_fp8_f32 v17, v32, v33
	v_pk_mul_f32 v[18:19], v[20:21], v[28:29]
	v_cvt_pk_fp8_f32 v16, v30, v31 op_sel:[0,0,1]
	v_pk_mul_f32 v[18:19], v[18:19], v[34:35]
	s_nop 0
	v_cvt_pk_fp8_f32 v17, v18, v19 op_sel:[0,0,1]
	s_waitcnt lgkmcnt(0)
; __device__ __forceinline__ float rstd_fin4(const f32x4 a) { float s = (a[0] + a[1]) + (a[2] + a[3]); s += __shfl_xor(s, 16); s += __shfl_xor(s, 32); return __builtin_amdgcn_rsqf(s * (1.f / 1024.f) + 1e-6f); }
;     __device__ __forceinline__ void operator()(const f32x4 (&acc)[2][2][4][2], const Unit& u, int wr, int wc, int fr, int fq) const {
;     ...
;             for (int m = 0; m < 4; ++m) { const float rs = rstd_fin4(pa[ai][m]) * sc;
;                 const float rsl = rs * 1.4426950408889634f, rsu = rs * 0.6931471805599453f;
;                 f32x4 h0, h1;
; #pragma unroll
;                 for (int n = 0; n < 2; ++n) { const f32x4 G = acc[ai][0][m][n], U = acc[ai][1][m][n]; f32x4 hv;
; #pragma unroll
;                     for (int q = 0; q < 2; ++q) { const f32x2 g2 = (f32x2){G[2 * q], G[2 * q + 1]} * rsl, u2 = (f32x2){U[2 * q], U[2 * q + 1]} * rsu;
;                         f32x2 r2; r2.x = __builtin_amdgcn_rcpf(1.f + __builtin_amdgcn_exp2f(-g2.x)); r2.y = __builtin_amdgcn_rcpf(1.f + __builtin_amdgcn_exp2f(-g2.y));
;                         const f32x2 o2 = g2 * u2 * r2; hv[2 * q] = o2.x; hv[2 * q + 1] = o2.y; }
;                     if (n == 0) h0 = hv; else h1 = hv; }
;                 unsigned w0 = 0u, w1 = 0u;
;                 w0 = __builtin_amdgcn_cvt_pk_fp8_f32(h0[0], h0[1], w0, false); w0 = __builtin_amdgcn_cvt_pk_fp8_f32(h0[2], h0[3], w0, true); w1 = __builtin_amdgcn_cvt_pk_fp8_f32(h1[0], h1[1], w1, false); w1 = __builtin_amdgcn_cvt_pk_fp8_f32(h1[2], h1[3], w1, true);
;                 *(u32x2*)(hb + (ai * 4 + m) * 512) = (u32x2){w0, w1}; asm volatile("" ::: "memory"); }
	v_add_f32_e32 v18, v22, v23
	v_fmamk_f32 v18, v18, 0x3a800000, v227
	v_rsq_f32_e32 v18, v18
	global_store_dwordx2 v[24:25], v[16:17], off offset:1536 nt
	v_mul_f32_e32 v17, 0x3c800000, v18
	v_mul_f32_e32 v16, 0x3fb8aa3b, v17
	v_pk_mul_f32 v[18:19], v[96:97], v[16:17] op_sel_hi:[1,0]
	v_mul_f32_e32 v20, 0x3f317218, v17
	v_exp_f32_e64 v21, -v18
	v_exp_f32_e64 v17, -v19
	v_pk_mul_f32 v[22:23], v[88:89], v[20:21] op_sel_hi:[1,0]
	v_add_f32_e32 v17, 1.0, v17
	v_pk_mul_f32 v[18:19], v[18:19], v[22:23]
	v_pk_mul_f32 v[22:23], v[98:99], v[16:17] op_sel_hi:[1,0]
	v_add_f32_e32 v21, 1.0, v21
	v_rcp_f32_e32 v29, v17
	v_exp_f32_e64 v17, -v22
	v_rcp_f32_e32 v28, v21
	v_exp_f32_e64 v21, -v23
	v_add_f32_e32 v17, 1.0, v17
	v_pk_mul_f32 v[18:19], v[18:19], v[28:29]
	v_pk_mul_f32 v[28:29], v[90:91], v[20:21] op_sel_hi:[1,0]
	v_rcp_f32_e32 v30, v17
	v_add_f32_e32 v17, 1.0, v21
	v_pk_mul_f32 v[22:23], v[22:23], v[28:29]
	v_pk_mul_f32 v[28:29], v[92:93], v[16:17] op_sel_hi:[1,0]
	v_rcp_f32_e32 v31, v17
	v_exp_f32_e64 v21, -v29
	v_exp_f32_e64 v17, -v28
	v_pk_mul_f32 v[22:23], v[22:23], v[30:31]
	v_pk_mul_f32 v[30:31], v[84:85], v[20:21] op_sel_hi:[1,0]
	v_add_f32_e32 v17, 1.0, v17
	v_pk_mul_f32 v[28:29], v[28:29], v[30:31]
	s_waitcnt vmcnt(6)
	v_mov_b32_e32 v30, v13
	v_mov_b32_e32 v31, v14
	v_mov_b32_e32 v13, v15
	v_pk_add_f32 v[12:13], v[30:31], v[12:13]
	v_rcp_f32_e32 v32, v17
	v_add_f32_e32 v30, v12, v13
	ds_bpermute_b32 v31, v27, v30
	v_add_f32_e32 v17, 1.0, v21
	v_rcp_f32_e32 v33, v17
	v_pk_mul_f32 v[16:17], v[94:95], v[16:17] op_sel_hi:[1,0]
	v_pk_mul_f32 v[20:21], v[86:87], v[20:21] op_sel_hi:[1,0]
	v_exp_f32_e64 v34, -v16
	v_pk_mul_f32 v[14:15], v[16:17], v[20:21]
	s_waitcnt lgkmcnt(0)
	v_add_f32_e32 v20, v30, v31
	ds_bpermute_b32 v21, v26, v20
	v_pk_mul_f32 v[28:29], v[28:29], v[32:33]
	v_exp_f32_e64 v33, -v17
	v_mov_b32_e32 v16, v3
	v_add_f32_e32 v32, 1.0, v34
	v_cvt_pk_fp8_f32 v16, v18, v19
	v_add_f32_e32 v13, 1.0, v33
	s_waitcnt lgkmcnt(0)
	v_add_f32_e32 v18, v20, v21
	v_rcp_f32_e32 v12, v32
	v_rcp_f32_e32 v13, v13
	v_mov_b32_e32 v17, v3
	v_fmamk_f32 v18, v18, 0x3a800000, v227
	v_cvt_pk_fp8_f32 v17, v28, v29
	v_rsq_f32_e32 v18, v18
	v_pk_mul_f32 v[12:13], v[14:15], v[12:13]
	v_cvt_pk_fp8_f32 v16, v22, v23 op_sel:[0,0,1]
	v_cvt_pk_fp8_f32 v17, v12, v13 op_sel:[0,0,1]
	v_mul_f32_e32 v13, 0x3c800000, v18
	v_mul_f32_e32 v12, 0x3fb8aa3b, v13
	v_pk_mul_f32 v[14:15], v[80:81], v[12:13] op_sel_hi:[1,0]
	v_mul_f32_e32 v18, 0x3f317218, v13
	v_exp_f32_e64 v19, -v14
	v_exp_f32_e64 v13, -v15
	global_store_dwordx2 v[24:25], v[16:17], off offset:2048 nt
	v_pk_mul_f32 v[20:21], v[72:73], v[18:19] op_sel_hi:[1,0]
	v_add_f32_e32 v13, 1.0, v13
	v_pk_mul_f32 v[14:15], v[14:15], v[20:21]
	v_pk_mul_f32 v[20:21], v[82:83], v[12:13] op_sel_hi:[1,0]
	v_add_f32_e32 v19, 1.0, v19
	v_rcp_f32_e32 v23, v13
	v_exp_f32_e64 v13, -v20
	v_rcp_f32_e32 v22, v19
	v_exp_f32_e64 v19, -v21
	v_add_f32_e32 v13, 1.0, v13
	v_pk_mul_f32 v[14:15], v[14:15], v[22:23]
	v_pk_mul_f32 v[22:23], v[74:75], v[18:19] op_sel_hi:[1,0]
	v_rcp_f32_e32 v28, v13
	v_add_f32_e32 v13, 1.0, v19
	v_pk_mul_f32 v[20:21], v[20:21], v[22:23]
	v_pk_mul_f32 v[22:23], v[76:77], v[12:13] op_sel_hi:[1,0]
	v_rcp_f32_e32 v29, v13
	v_exp_f32_e64 v13, -v22
	v_exp_f32_e64 v19, -v23
	v_pk_mul_f32 v[20:21], v[20:21], v[28:29]
	v_add_f32_e32 v13, 1.0, v13
	v_rcp_f32_e32 v30, v13
	v_add_f32_e32 v13, 1.0, v19
	v_rcp_f32_e32 v31, v13
	v_pk_mul_f32 v[28:29], v[68:69], v[18:19] op_sel_hi:[1,0]
	v_pk_mul_f32 v[12:13], v[78:79], v[12:13] op_sel_hi:[1,0]
	v_pk_mul_f32 v[22:23], v[22:23], v[28:29]
	v_exp_f32_e64 v28, -v12
	v_pk_mul_f32 v[22:23], v[22:23], v[30:31]
	s_waitcnt vmcnt(6)
	v_mov_b32_e32 v30, v9
	v_mov_b32_e32 v31, v10
	v_mov_b32_e32 v9, v11
	v_pk_add_f32 v[8:9], v[30:31], v[8:9]
	v_exp_f32_e64 v29, -v13
	v_add_f32_e32 v10, v8, v9
	ds_bpermute_b32 v11, v27, v10
	v_mov_b32_e32 v8, v3
	v_add_f32_e32 v28, 1.0, v28
	v_add_f32_e32 v29, 1.0, v29
	v_cvt_pk_fp8_f32 v8, v14, v15
	s_waitcnt lgkmcnt(0)
	v_add_f32_e32 v14, v10, v11
	v_rcp_f32_e32 v28, v28
	v_rcp_f32_e32 v29, v29
	v_mov_b32_e32 v9, v3
	ds_bpermute_b32 v15, v26, v14
	v_cvt_pk_fp8_f32 v9, v22, v23
	v_pk_mul_f32 v[18:19], v[70:71], v[18:19] op_sel_hi:[1,0]
	v_cvt_pk_fp8_f32 v8, v20, v21 op_sel:[0,0,1]
	v_pk_mul_f32 v[10:11], v[12:13], v[18:19]
	s_nop 0
	v_pk_mul_f32 v[10:11], v[10:11], v[28:29]
	s_nop 0
	v_cvt_pk_fp8_f32 v9, v10, v11 op_sel:[0,0,1]
	s_waitcnt lgkmcnt(0)
; __device__ __forceinline__ float rstd_fin4(const f32x4 a) { float s = (a[0] + a[1]) + (a[2] + a[3]); s += __shfl_xor(s, 16); s += __shfl_xor(s, 32); return __builtin_amdgcn_rsqf(s * (1.f / 1024.f) + 1e-6f); }
;     __device__ __forceinline__ void operator()(const f32x4 (&acc)[2][2][4][2], const Unit& u, int wr, int wc, int fr, int fq) const {
;     ...
;             for (int m = 0; m < 4; ++m) { const float rs = rstd_fin4(pa[ai][m]) * sc;
;                 const float rsl = rs * 1.4426950408889634f, rsu = rs * 0.6931471805599453f;
;                 f32x4 h0, h1;
; #pragma unroll
;                 for (int n = 0; n < 2; ++n) { const f32x4 G = acc[ai][0][m][n], U = acc[ai][1][m][n]; f32x4 hv;
; #pragma unroll
;                     for (int q = 0; q < 2; ++q) { const f32x2 g2 = (f32x2){G[2 * q], G[2 * q + 1]} * rsl, u2 = (f32x2){U[2 * q], U[2 * q + 1]} * rsu;
;                         f32x2 r2; r2.x = __builtin_amdgcn_rcpf(1.f + __builtin_amdgcn_exp2f(-g2.x)); r2.y = __builtin_amdgcn_rcpf(1.f + __builtin_amdgcn_exp2f(-g2.y));
;                         const f32x2 o2 = g2 * u2 * r2; hv[2 * q] = o2.x; hv[2 * q + 1] = o2.y; }
;                     if (n == 0) h0 = hv; else h1 = hv; }
;                 unsigned w0 = 0u, w1 = 0u;
;                 w0 = __builtin_amdgcn_cvt_pk_fp8_f32(h0[0], h0[1], w0, false); w0 = __builtin_amdgcn_cvt_pk_fp8_f32(h0[2], h0[3], w0, true); w1 = __builtin_amdgcn_cvt_pk_fp8_f32(h1[0], h1[1], w1, false); w1 = __builtin_amdgcn_cvt_pk_fp8_f32(h1[2], h1[3], w1, true);
;                 *(u32x2*)(hb + (ai * 4 + m) * 512) = (u32x2){w0, w1}; asm volatile("" ::: "memory"); }
	v_add_f32_e32 v10, v14, v15
	v_fmamk_f32 v10, v10, 0x3a800000, v227
	v_rsq_f32_e32 v10, v10
	global_store_dwordx2 v[24:25], v[8:9], off offset:2560 nt
	v_mul_f32_e32 v9, 0x3c800000, v10
	v_mul_f32_e32 v8, 0x3fb8aa3b, v9
	v_pk_mul_f32 v[10:11], v[64:65], v[8:9] op_sel_hi:[1,0]
	v_mul_f32_e32 v12, 0x3f317218, v9
	v_exp_f32_e64 v13, -v10
	v_exp_f32_e64 v9, -v11
	v_pk_mul_f32 v[14:15], v[56:57], v[12:13] op_sel_hi:[1,0]
	v_add_f32_e32 v9, 1.0, v9
	v_pk_mul_f32 v[10:11], v[10:11], v[14:15]
	v_pk_mul_f32 v[14:15], v[66:67], v[8:9] op_sel_hi:[1,0]
	v_add_f32_e32 v13, 1.0, v13
	v_rcp_f32_e32 v17, v9
	v_exp_f32_e64 v9, -v14
	v_rcp_f32_e32 v16, v13
	v_exp_f32_e64 v13, -v15
	v_add_f32_e32 v9, 1.0, v9
	v_pk_mul_f32 v[10:11], v[10:11], v[16:17]
	v_pk_mul_f32 v[16:17], v[58:59], v[12:13] op_sel_hi:[1,0]
	v_rcp_f32_e32 v18, v9
	v_add_f32_e32 v9, 1.0, v13
	v_pk_mul_f32 v[14:15], v[14:15], v[16:17]
	v_pk_mul_f32 v[16:17], v[60:61], v[8:9] op_sel_hi:[1,0]
	v_rcp_f32_e32 v19, v9
	v_exp_f32_e64 v13, -v17
	v_exp_f32_e64 v9, -v16
	v_pk_mul_f32 v[14:15], v[14:15], v[18:19]
	v_pk_mul_f32 v[18:19], v[52:53], v[12:13] op_sel_hi:[1,0]
	v_add_f32_e32 v9, 1.0, v9
	v_pk_mul_f32 v[16:17], v[16:17], v[18:19]
	s_waitcnt vmcnt(6)
	v_mov_b32_e32 v18, v5
	v_mov_b32_e32 v19, v6
	v_mov_b32_e32 v5, v7
	v_pk_add_f32 v[4:5], v[18:19], v[4:5]
	v_rcp_f32_e32 v20, v9
	v_add_f32_e32 v18, v4, v5
	ds_bpermute_b32 v19, v27, v18
	v_add_f32_e32 v9, 1.0, v13
	v_rcp_f32_e32 v21, v9
	v_pk_mul_f32 v[8:9], v[62:63], v[8:9] op_sel_hi:[1,0]
	v_pk_mul_f32 v[12:13], v[54:55], v[12:13] op_sel_hi:[1,0]
	v_exp_f32_e64 v22, -v8
	v_pk_mul_f32 v[6:7], v[8:9], v[12:13]
	s_waitcnt lgkmcnt(0)
	v_add_f32_e32 v12, v18, v19
	ds_bpermute_b32 v13, v26, v12
	v_pk_mul_f32 v[16:17], v[16:17], v[20:21]
	v_exp_f32_e64 v21, -v9
	v_mov_b32_e32 v8, v3
	v_add_f32_e32 v20, 1.0, v22
	v_cvt_pk_fp8_f32 v8, v10, v11
	v_add_f32_e32 v5, 1.0, v21
	s_waitcnt lgkmcnt(0)
	v_add_f32_e32 v10, v12, v13
	v_rcp_f32_e32 v4, v20
	v_rcp_f32_e32 v5, v5
	v_mov_b32_e32 v9, v3
	v_fmamk_f32 v10, v10, 0x3a800000, v227
	v_cvt_pk_fp8_f32 v9, v16, v17
	v_rsq_f32_e32 v10, v10
	v_pk_mul_f32 v[4:5], v[6:7], v[4:5]
	v_cvt_pk_fp8_f32 v8, v14, v15 op_sel:[0,0,1]
	v_cvt_pk_fp8_f32 v9, v4, v5 op_sel:[0,0,1]
	v_mul_f32_e32 v5, 0x3c800000, v10
	v_mul_f32_e32 v4, 0x3fb8aa3b, v5
	v_pk_mul_f32 v[6:7], v[48:49], v[4:5] op_sel_hi:[1,0]
	v_mul_f32_e32 v10, 0x3f317218, v5
	v_exp_f32_e64 v11, -v6
	v_exp_f32_e64 v5, -v7
	global_store_dwordx2 v[24:25], v[8:9], off offset:3072 nt
	v_pk_mul_f32 v[12:13], v[40:41], v[10:11] op_sel_hi:[1,0]
	v_add_f32_e32 v5, 1.0, v5
	v_pk_mul_f32 v[6:7], v[6:7], v[12:13]
	v_pk_mul_f32 v[12:13], v[50:51], v[4:5] op_sel_hi:[1,0]
	v_add_f32_e32 v11, 1.0, v11
	v_rcp_f32_e32 v15, v5
	v_exp_f32_e64 v5, -v12
	v_rcp_f32_e32 v14, v11
	v_exp_f32_e64 v11, -v13
	v_add_f32_e32 v5, 1.0, v5
	v_pk_mul_f32 v[6:7], v[6:7], v[14:15]
	v_pk_mul_f32 v[14:15], v[42:43], v[10:11] op_sel_hi:[1,0]
	v_rcp_f32_e32 v16, v5
	v_add_f32_e32 v5, 1.0, v11
	v_pk_mul_f32 v[12:13], v[12:13], v[14:15]
	v_pk_mul_f32 v[14:15], v[44:45], v[4:5] op_sel_hi:[1,0]
	v_rcp_f32_e32 v17, v5
	v_exp_f32_e64 v5, -v14
	v_exp_f32_e64 v11, -v15
	v_pk_mul_f32 v[12:13], v[12:13], v[16:17]
	v_add_f32_e32 v5, 1.0, v5
	v_rcp_f32_e32 v18, v5
	v_add_f32_e32 v5, 1.0, v11
	v_pk_mul_f32 v[16:17], v[36:37], v[10:11] op_sel_hi:[1,0]
	v_rcp_f32_e32 v19, v5
	v_pk_mul_f32 v[4:5], v[46:47], v[4:5] op_sel_hi:[1,0]
	v_pk_mul_f32 v[14:15], v[14:15], v[16:17]
	v_exp_f32_e64 v16, -v4
	v_exp_f32_e64 v17, -v5
	v_pk_mul_f32 v[14:15], v[14:15], v[18:19]
	v_mov_b32_e32 v18, v3
	v_add_f32_e32 v16, 1.0, v16
	v_add_f32_e32 v17, 1.0, v17
	v_rcp_f32_e32 v16, v16
	v_rcp_f32_e32 v17, v17
	v_mov_b32_e32 v19, v3
	v_cvt_pk_fp8_f32 v18, v6, v7
	v_cvt_pk_fp8_f32 v19, v14, v15
	v_pk_mul_f32 v[10:11], v[38:39], v[10:11] op_sel_hi:[1,0]
	v_cvt_pk_fp8_f32 v18, v12, v13 op_sel:[0,0,1]
	v_pk_mul_f32 v[4:5], v[4:5], v[10:11]
	s_nop 0
	v_pk_mul_f32 v[4:5], v[4:5], v[16:17]
	s_nop 0
	v_cvt_pk_fp8_f32 v19, v4, v5 op_sel:[0,0,1]
	global_store_dwordx2 v[24:25], v[18:19], off offset:3584 nt
	s_cbranch_vccnz .LBB0_1667
	s_andn2_b64 vcc, exec, s[48:49]
	s_cbranch_vccnz .LBB0_1666
	s_barrier
	s_branch .LBB0_1666

; __device__ __forceinline__ float rstd_fin4(const f32x4 a) { float s = (a[0] + a[1]) + (a[2] + a[3]); s += __shfl_xor(s, 16); s += __shfl_xor(s, 32); return __builtin_amdgcn_rsqf(s * (1.f / 1024.f) + 1e-6f); }
;     __device__ __forceinline__ void operator()(const f32x4 (&acc)[2][2][4][2], const Unit& u, int wr, int wc, int fr, int fq) const {
;     ...
;         const int row0 = u.pm * BM + wr * 64 + fr;
;         unsigned char* const hb = (unsigned char*)H + (size_t)(u.pm * (FFH / 128) + u.pn + pn0) * 32768 + (((wr * 4 + wc) * 8) * 64 + (fq >> 1) * 32 + fr * 2 + (fq & 1)) * 8;
;         f32x4 pa[2][4];
; #pragma unroll
;         for (int ai = 0; ai < 2; ++ai)
; #pragma unroll
;             for (int m = 0; m < 4; ++m) pa[ai][m] = rstd_ld4(ss, row0 + ai * HALF + m * 16, fq);
; #pragma unroll
;         for (int ai = 0; ai < 2; ++ai)
; #pragma unroll
;             for (int m = 0; m < 4; ++m) { const float rs = rstd_fin4(pa[ai][m]) * sc;
;                 const float rsl = rs * 1.4426950408889634f, rsu = rs * 0.6931471805599453f;
;                 f32x4 h0, h1;
; #pragma unroll
;                 for (int n = 0; n < 2; ++n) { const f32x4 G = acc[ai][0][m][n], U = acc[ai][1][m][n]; f32x4 hv;
; #pragma unroll
;                     for (int q = 0; q < 2; ++q) { const f32x2 g2 = (f32x2){G[2 * q], G[2 * q + 1]} * rsl, u2 = (f32x2){U[2 * q], U[2 * q + 1]} * rsu;
;                         f32x2 r2; r2.x = __builtin_amdgcn_rcpf(1.f + __builtin_amdgcn_exp2f(-g2.x)); r2.y = __builtin_amdgcn_rcpf(1.f + __builtin_amdgcn_exp2f(-g2.y));
.LBB0_1692:
	s_lshl_b32 s4, s68, 8
	v_mov_b32_e32 v14, v1
	v_mov_b32_e32 v15, v182
	s_add_i32 s4, s4, s62
	v_and_b32_e32 v17, 64, v246
	v_add_u32_e32 v4, s4, v14
	v_lshlrev_b32_e32 v6, 2, v15
	v_ashrrev_i32_e32 v7, 31, v6
	v_ashrrev_i32_e32 v5, 31, v4
	v_lshl_add_u64 v[6:7], v[6:7], 2, s[42:43]
	v_lshlrev_b64 v[4:5], 6, v[4:5]
	v_lshl_add_u64 v[12:13], v[6:7], 0, v[4:5]
	global_load_dwordx4 v[4:7], v[12:13], off
	global_load_dwordx4 v[8:11], v[12:13], off offset:1024
	global_load_dwordx4 v[28:31], v[12:13], off offset:2048
	global_load_dwordx4 v[20:23], v[12:13], off offset:3072
	v_xor_b32_e32 v16, 16, v246
	v_add_u32_e32 v17, 64, v17
	v_xor_b32_e32 v18, 32, v246
	v_cmp_lt_i32_e32 vcc, v16, v17
	v_mov_b32_e32 v32, v3
	v_mov_b32_e32 v33, v3
	v_cndmask_b32_e32 v16, v246, v16, vcc
	v_cmp_lt_i32_e32 vcc, v18, v17
	v_lshlrev_b32_e32 v27, 2, v16
	s_mul_i32 s4, s68, 22
	v_cndmask_b32_e32 v17, v246, v18, vcc
	v_lshlrev_b32_e32 v26, 2, v17
	s_add_i32 s4, s4, s67
	s_ashr_i32 s5, s4, 31
	v_lshlrev_b32_e32 v19, 4, v15
	v_lshl_add_u32 v14, v14, 1, s65
	s_lshl_b64 s[4:5], s[4:5], 15
	v_and_b32_e32 v18, 0x1fffffe0, v19
	v_and_or_b32 v14, v15, 1, v14
	v_add_lshl_u32 v14, v14, v18, 3
	s_add_u32 s4, s22, s4
	v_ashrrev_i32_e32 v15, 31, v14
	s_addc_u32 s5, s23, s5
	v_lshl_add_u64 v[24:25], s[4:5], 0, v[14:15]
	s_mov_b64 s[4:5], -1
	s_waitcnt vmcnt(0)
	v_mov_b32_e32 v16, v5
	v_mov_b32_e32 v17, v6
	v_mov_b32_e32 v5, v7
	v_mov_b32_e32 v6, v9
	v_mov_b32_e32 v7, v10
	v_mov_b32_e32 v9, v11
	v_pk_add_f32 v[4:5], v[16:17], v[4:5]
	v_pk_add_f32 v[6:7], v[6:7], v[8:9]
	v_add_f32_e32 v8, v4, v5
	v_add_f32_e32 v6, v6, v7
	ds_bpermute_b32 v7, v27, v8
	ds_bpermute_b32 v9, v27, v6
	v_add_co_u32_e32 v4, vcc, s88, v12
	s_waitcnt lgkmcnt(1)
	v_add_f32_e32 v7, v8, v7
	s_waitcnt lgkmcnt(0)
	v_add_f32_e32 v6, v6, v9
	ds_bpermute_b32 v8, v26, v7
	ds_bpermute_b32 v9, v26, v6
	v_addc_co_u32_e32 v5, vcc, 0, v13, vcc
	global_load_dwordx4 v[16:19], v[4:5], off
	global_load_dwordx4 v[12:15], v[4:5], off offset:1024
	s_waitcnt lgkmcnt(1)
	v_add_f32_e32 v7, v7, v8
	s_waitcnt lgkmcnt(0)
	v_add_f32_e32 v6, v6, v9
	v_fmamk_f32 v7, v7, 0x3a800000, v227
	v_fmamk_f32 v6, v6, 0x3a800000, v227
	v_rsq_f32_e32 v34, v7
	v_rsq_f32_e32 v35, v6
	global_load_dwordx4 v[8:11], v[4:5], off offset:2048
	s_nop 0
	global_load_dwordx4 v[4:7], v[4:5], off offset:3072
	s_andn2_b64 vcc, exec, s[40:41]
	v_mul_f32_e32 v174, 0x3c800000, v34
	v_mul_f32_e32 v35, 0x3c800000, v35
	v_mul_f32_e32 v34, 0x3fb8aa3b, v174
	v_mul_f32_e32 v174, 0x3f317218, v174
	v_pk_mul_f32 v[160:161], v[160:161], v[34:35] op_sel_hi:[1,0]
	v_pk_mul_f32 v[152:153], v[152:153], v[174:175] op_sel_hi:[1,0]
	v_pk_mul_f32 v[162:163], v[162:163], v[34:35] op_sel_hi:[1,0]
	v_pk_mul_f32 v[154:155], v[154:155], v[174:175] op_sel_hi:[1,0]
	v_pk_mul_f32 v[156:157], v[156:157], v[34:35] op_sel_hi:[1,0]
	v_mul_f32_e32 v176, 0x3fb8aa3b, v35
	v_mul_f32_e32 v178, 0x3f317218, v35
	v_pk_mul_f32 v[148:149], v[148:149], v[174:175] op_sel_hi:[1,0]
	v_pk_mul_f32 v[34:35], v[158:159], v[34:35] op_sel_hi:[1,0]
	v_exp_f32_e64 v158, -v160
	v_exp_f32_e64 v159, -v161
	v_pk_mul_f32 v[152:153], v[160:161], v[152:153]
	v_exp_f32_e64 v160, -v162
	v_exp_f32_e64 v161, -v163
	v_pk_mul_f32 v[154:155], v[162:163], v[154:155]
	v_exp_f32_e64 v162, -v156
	v_exp_f32_e64 v163, -v157
	v_pk_mul_f32 v[148:149], v[156:157], v[148:149]
	v_exp_f32_e64 v156, -v34
	v_exp_f32_e64 v157, -v35
	v_pk_mul_f32 v[150:151], v[150:151], v[174:175] op_sel_hi:[1,0]
	v_pk_mul_f32 v[144:145], v[144:145], v[176:177] op_sel_hi:[1,0]
	v_pk_mul_f32 v[34:35], v[34:35], v[150:151]
	v_add_f32_e32 v150, 1.0, v158
	v_add_f32_e32 v151, 1.0, v159
	v_add_f32_e32 v158, 1.0, v160
	v_add_f32_e32 v159, 1.0, v161
	v_add_f32_e32 v160, 1.0, v162
	v_add_f32_e32 v161, 1.0, v163
	v_add_f32_e32 v162, 1.0, v156
	v_add_f32_e32 v163, 1.0, v157
	v_rcp_f32_e32 v150, v150
	v_rcp_f32_e32 v151, v151
	v_rcp_f32_e32 v156, v158
	v_rcp_f32_e32 v157, v159
	v_rcp_f32_e32 v158, v160
	v_rcp_f32_e32 v159, v161
	v_rcp_f32_e32 v160, v162
	v_rcp_f32_e32 v161, v163
	v_pk_mul_f32 v[150:151], v[152:153], v[150:151]
	v_pk_mul_f32 v[148:149], v[148:149], v[158:159]
	v_cvt_pk_fp8_f32 v32, v150, v151
	v_cvt_pk_fp8_f32 v33, v148, v149
	v_pk_mul_f32 v[148:149], v[154:155], v[156:157]
	v_pk_mul_f32 v[34:35], v[34:35], v[160:161]
	v_cvt_pk_fp8_f32 v32, v148, v149 op_sel:[0,0,1]
	v_cvt_pk_fp8_f32 v33, v34, v35 op_sel:[0,0,1]
	v_exp_f32_e64 v35, -v145
	v_exp_f32_e64 v174, -v144
	v_pk_mul_f32 v[136:137], v[136:137], v[178:179] op_sel_hi:[1,0]
	global_store_dwordx2 v[24:25], v[32:33], off nt
	v_add_f32_e32 v32, 1.0, v35
	v_add_f32_e32 v34, 1.0, v174
	v_rcp_f32_e32 v35, v32
	v_pk_mul_f32 v[32:33], v[144:145], v[136:137]
	v_pk_mul_f32 v[136:137], v[146:147], v[176:177] op_sel_hi:[1,0]
	v_rcp_f32_e32 v34, v34
	v_exp_f32_e64 v144, -v136
	v_exp_f32_e64 v145, -v137
	v_pk_mul_f32 v[132:133], v[132:133], v[178:179] op_sel_hi:[1,0]
	v_pk_mul_f32 v[32:33], v[32:33], v[34:35]
	v_pk_mul_f32 v[34:35], v[138:139], v[178:179] op_sel_hi:[1,0]
	v_add_f32_e32 v138, 1.0, v144
	v_add_f32_e32 v139, 1.0, v145
	v_rcp_f32_e32 v138, v138
	v_rcp_f32_e32 v139, v139
	v_pk_mul_f32 v[34:35], v[136:137], v[34:35]
	v_pk_mul_f32 v[136:137], v[140:141], v[176:177] op_sel_hi:[1,0]
	v_pk_mul_f32 v[134:135], v[134:135], v[178:179] op_sel_hi:[1,0]
	v_exp_f32_e64 v140, -v136
	v_pk_mul_f32 v[34:35], v[34:35], v[138:139]
	v_exp_f32_e64 v139, -v137
	v_pk_mul_f32 v[132:133], v[136:137], v[132:133]
	v_mov_b32_e32 v136, v29
	v_mov_b32_e32 v137, v30
	v_mov_b32_e32 v29, v31
	v_pk_add_f32 v[28:29], v[136:137], v[28:29]
	v_add_f32_e32 v138, 1.0, v140
	v_add_f32_e32 v136, v28, v29
	ds_bpermute_b32 v137, v27, v136
	v_add_f32_e32 v139, 1.0, v139
	v_rcp_f32_e32 v138, v138
	v_rcp_f32_e32 v139, v139
	v_pk_mul_f32 v[140:141], v[142:143], v[176:177] op_sel_hi:[1,0]
	s_waitcnt lgkmcnt(0)
; __device__ __forceinline__ float rstd_fin4(const f32x4 a) { float s = (a[0] + a[1]) + (a[2] + a[3]); s += __shfl_xor(s, 16); s += __shfl_xor(s, 32); return __builtin_amdgcn_rsqf(s * (1.f / 1024.f) + 1e-6f); }
;     __device__ __forceinline__ void operator()(const f32x4 (&acc)[2][2][4][2], const Unit& u, int wr, int wc, int fr, int fq) const {
;     ...
;             for (int m = 0; m < 4; ++m) { const float rs = rstd_fin4(pa[ai][m]) * sc;
;                 const float rsl = rs * 1.4426950408889634f, rsu = rs * 0.6931471805599453f;
;                 f32x4 h0, h1;
; #pragma unroll
;                 for (int n = 0; n < 2; ++n) { const f32x4 G = acc[ai][0][m][n], U = acc[ai][1][m][n]; f32x4 hv;
; #pragma unroll
;                     for (int q = 0; q < 2; ++q) { const f32x2 g2 = (f32x2){G[2 * q], G[2 * q + 1]} * rsl, u2 = (f32x2){U[2 * q], U[2 * q + 1]} * rsu;
;                         f32x2 r2; r2.x = __builtin_amdgcn_rcpf(1.f + __builtin_amdgcn_exp2f(-g2.x)); r2.y = __builtin_amdgcn_rcpf(1.f + __builtin_amdgcn_exp2f(-g2.y));
;                         const f32x2 o2 = g2 * u2 * r2; hv[2 * q] = o2.x; hv[2 * q + 1] = o2.y; }
;                     if (n == 0) h0 = hv; else h1 = hv; }
;                 unsigned w0 = 0u, w1 = 0u;
;                 w0 = __builtin_amdgcn_cvt_pk_fp8_f32(h0[0], h0[1], w0, false); w0 = __builtin_amdgcn_cvt_pk_fp8_f32(h0[2], h0[3], w0, true); w1 = __builtin_amdgcn_cvt_pk_fp8_f32(h1[0], h1[1], w1, false); w1 = __builtin_amdgcn_cvt_pk_fp8_f32(h1[2], h1[3], w1, true);
;                 *(u32x2*)(hb + (ai * 4 + m) * 512) = (u32x2){w0, w1}; asm volatile("" ::: "memory"); }
	v_add_f32_e32 v136, v136, v137
	ds_bpermute_b32 v137, v26, v136
	v_exp_f32_e64 v142, -v140
	v_pk_mul_f32 v[132:133], v[132:133], v[138:139]
	v_exp_f32_e64 v139, -v141
	v_pk_mul_f32 v[30:31], v[140:141], v[134:135]
	v_mov_b32_e32 v134, v3
	v_add_f32_e32 v138, 1.0, v142
	v_add_f32_e32 v29, 1.0, v139
	v_cvt_pk_fp8_f32 v134, v32, v33
	s_waitcnt lgkmcnt(0)
	v_add_f32_e32 v32, v136, v137
	v_rcp_f32_e32 v28, v138
	v_rcp_f32_e32 v29, v29
	v_mov_b32_e32 v135, v3
	v_fmamk_f32 v32, v32, 0x3a800000, v227
	v_cvt_pk_fp8_f32 v135, v132, v133
	v_rsq_f32_e32 v32, v32
	v_pk_mul_f32 v[28:29], v[30:31], v[28:29]
	v_cvt_pk_fp8_f32 v134, v34, v35 op_sel:[0,0,1]
	v_cvt_pk_fp8_f32 v135, v28, v29 op_sel:[0,0,1]
	v_mul_f32_e32 v29, 0x3c800000, v32
	v_mul_f32_e32 v28, 0x3fb8aa3b, v29
	v_pk_mul_f32 v[30:31], v[128:129], v[28:29] op_sel_hi:[1,0]
	v_mul_f32_e32 v32, 0x3f317218, v29
	v_exp_f32_e64 v33, -v30
	v_exp_f32_e64 v29, -v31
	global_store_dwordx2 v[24:25], v[134:135], off offset:512 nt
	v_pk_mul_f32 v[34:35], v[120:121], v[32:33] op_sel_hi:[1,0]
	v_add_f32_e32 v29, 1.0, v29
	v_pk_mul_f32 v[30:31], v[30:31], v[34:35]
	v_pk_mul_f32 v[34:35], v[130:131], v[28:29] op_sel_hi:[1,0]
	v_add_f32_e32 v33, 1.0, v33
	v_rcp_f32_e32 v121, v29
	v_exp_f32_e64 v29, -v34
	v_rcp_f32_e32 v120, v33
	v_exp_f32_e64 v33, -v35
	v_add_f32_e32 v29, 1.0, v29
	v_pk_mul_f32 v[30:31], v[30:31], v[120:121]
	v_pk_mul_f32 v[120:121], v[122:123], v[32:33] op_sel_hi:[1,0]
	v_rcp_f32_e32 v122, v29
	v_add_f32_e32 v29, 1.0, v33
	v_pk_mul_f32 v[34:35], v[34:35], v[120:121]
	v_pk_mul_f32 v[120:121], v[124:125], v[28:29] op_sel_hi:[1,0]
	v_rcp_f32_e32 v123, v29
	v_exp_f32_e64 v29, -v120
	v_exp_f32_e64 v33, -v121
	v_pk_mul_f32 v[34:35], v[34:35], v[122:123]
	v_add_f32_e32 v29, 1.0, v29
	v_rcp_f32_e32 v122, v29
	v_add_f32_e32 v29, 1.0, v33
	v_pk_mul_f32 v[116:117], v[116:117], v[32:33] op_sel_hi:[1,0]
	v_rcp_f32_e32 v123, v29
	v_pk_mul_f32 v[28:29], v[126:127], v[28:29] op_sel_hi:[1,0]
	v_pk_mul_f32 v[116:117], v[120:121], v[116:117]
	v_exp_f32_e64 v120, -v28
	v_exp_f32_e64 v121, -v29
	v_pk_mul_f32 v[32:33], v[118:119], v[32:33] op_sel_hi:[1,0]
	v_pk_mul_f32 v[116:117], v[116:117], v[122:123]
	v_add_f32_e32 v118, 1.0, v120
	v_add_f32_e32 v119, 1.0, v121
	v_mov_b32_e32 v120, v21
	v_mov_b32_e32 v121, v22
	v_mov_b32_e32 v21, v23
	v_pk_add_f32 v[20:21], v[120:121], v[20:21]
	v_rcp_f32_e32 v118, v118
	v_add_f32_e32 v22, v20, v21
	ds_bpermute_b32 v23, v27, v22
	v_mov_b32_e32 v20, v3
	v_cvt_pk_fp8_f32 v20, v30, v31
	v_rcp_f32_e32 v119, v119
	v_mov_b32_e32 v21, v3
	s_waitcnt lgkmcnt(0)
	v_add_f32_e32 v30, v22, v23
	ds_bpermute_b32 v31, v26, v30
	v_cvt_pk_fp8_f32 v21, v116, v117
	v_pk_mul_f32 v[22:23], v[28:29], v[32:33]
	v_cvt_pk_fp8_f32 v20, v34, v35 op_sel:[0,0,1]
	v_pk_mul_f32 v[22:23], v[22:23], v[118:119]
	s_nop 0
	v_cvt_pk_fp8_f32 v21, v22, v23 op_sel:[0,0,1]
	s_waitcnt lgkmcnt(0)
	v_add_f32_e32 v22, v30, v31
	v_fmamk_f32 v22, v22, 0x3a800000, v227
	v_rsq_f32_e32 v22, v22
	global_store_dwordx2 v[24:25], v[20:21], off offset:1024 nt
	v_mul_f32_e32 v21, 0x3c800000, v22
	v_mul_f32_e32 v20, 0x3fb8aa3b, v21
	v_pk_mul_f32 v[22:23], v[112:113], v[20:21] op_sel_hi:[1,0]
	v_mul_f32_e32 v28, 0x3f317218, v21
	v_exp_f32_e64 v29, -v22
	v_exp_f32_e64 v21, -v23
	v_pk_mul_f32 v[30:31], v[104:105], v[28:29] op_sel_hi:[1,0]
	v_add_f32_e32 v21, 1.0, v21
	v_pk_mul_f32 v[22:23], v[22:23], v[30:31]
	v_pk_mul_f32 v[30:31], v[114:115], v[20:21] op_sel_hi:[1,0]
	v_add_f32_e32 v29, 1.0, v29
	v_rcp_f32_e32 v33, v21
	v_exp_f32_e64 v21, -v30
	v_rcp_f32_e32 v32, v29
	v_exp_f32_e64 v29, -v31
	v_add_f32_e32 v21, 1.0, v21
	v_pk_mul_f32 v[22:23], v[22:23], v[32:33]
	v_pk_mul_f32 v[32:33], v[106:107], v[28:29] op_sel_hi:[1,0]
	v_rcp_f32_e32 v34, v21
	v_add_f32_e32 v21, 1.0, v29
	v_pk_mul_f32 v[30:31], v[30:31], v[32:33]
	v_pk_mul_f32 v[32:33], v[108:109], v[20:21] op_sel_hi:[1,0]
	v_rcp_f32_e32 v35, v21
	v_exp_f32_e64 v21, -v32
	v_exp_f32_e64 v29, -v33
	v_pk_mul_f32 v[30:31], v[30:31], v[34:35]
	v_add_f32_e32 v21, 1.0, v21
	v_pk_mul_f32 v[34:35], v[100:101], v[28:29] op_sel_hi:[1,0]
	v_rcp_f32_e32 v100, v21
	v_add_f32_e32 v21, 1.0, v29
	v_rcp_f32_e32 v101, v21
	v_pk_mul_f32 v[32:33], v[32:33], v[34:35]
	v_pk_mul_f32 v[20:21], v[110:111], v[20:21] op_sel_hi:[1,0]
	v_pk_mul_f32 v[28:29], v[102:103], v[28:29] op_sel_hi:[1,0]
	v_pk_mul_f32 v[32:33], v[32:33], v[100:101]
	s_waitcnt vmcnt(6)
	v_mov_b32_e32 v100, v17
	v_mov_b32_e32 v101, v18
	v_mov_b32_e32 v17, v19
	v_pk_add_f32 v[16:17], v[100:101], v[16:17]
	v_exp_f32_e64 v34, -v20
	v_add_f32_e32 v18, v16, v17
	ds_bpermute_b32 v19, v27, v18
	v_exp_f32_e64 v35, -v21
	v_mov_b32_e32 v16, v3
	v_add_f32_e32 v34, 1.0, v34
	v_cvt_pk_fp8_f32 v16, v22, v23
	v_add_f32_e32 v35, 1.0, v35
	s_waitcnt lgkmcnt(0)
	v_add_f32_e32 v22, v18, v19
	v_rcp_f32_e32 v34, v34
	v_rcp_f32_e32 v35, v35
	v_mov_b32_e32 v17, v3
	ds_bpermute_b32 v23, v26, v22
	v_cvt_pk_fp8_f32 v17, v32, v33
	v_pk_mul_f32 v[18:19], v[20:21], v[28:29]
	v_cvt_pk_fp8_f32 v16, v30, v31 op_sel:[0,0,1]
	v_pk_mul_f32 v[18:19], v[18:19], v[34:35]
	s_nop 0
	v_cvt_pk_fp8_f32 v17, v18, v19 op_sel:[0,0,1]
	s_waitcnt lgkmcnt(0)
; __device__ __forceinline__ float rstd_fin4(const f32x4 a) { float s = (a[0] + a[1]) + (a[2] + a[3]); s += __shfl_xor(s, 16); s += __shfl_xor(s, 32); return __builtin_amdgcn_rsqf(s * (1.f / 1024.f) + 1e-6f); }
;     __device__ __forceinline__ void operator()(const f32x4 (&acc)[2][2][4][2], const Unit& u, int wr, int wc, int fr, int fq) const {
;     ...
;             for (int m = 0; m < 4; ++m) { const float rs = rstd_fin4(pa[ai][m]) * sc;
;                 const float rsl = rs * 1.4426950408889634f, rsu = rs * 0.6931471805599453f;
;                 f32x4 h0, h1;
; #pragma unroll
;                 for (int n = 0; n < 2; ++n) { const f32x4 G = acc[ai][0][m][n], U = acc[ai][1][m][n]; f32x4 hv;
; #pragma unroll
;                     for (int q = 0; q < 2; ++q) { const f32x2 g2 = (f32x2){G[2 * q], G[2 * q + 1]} * rsl, u2 = (f32x2){U[2 * q], U[2 * q + 1]} * rsu;
;                         f32x2 r2; r2.x = __builtin_amdgcn_rcpf(1.f + __builtin_amdgcn_exp2f(-g2.x)); r2.y = __builtin_amdgcn_rcpf(1.f + __builtin_amdgcn_exp2f(-g2.y));
;                         const f32x2 o2 = g2 * u2 * r2; hv[2 * q] = o2.x; hv[2 * q + 1] = o2.y; }
;                     if (n == 0) h0 = hv; else h1 = hv; }
;                 unsigned w0 = 0u, w1 = 0u;
;                 w0 = __builtin_amdgcn_cvt_pk_fp8_f32(h0[0], h0[1], w0, false); w0 = __builtin_amdgcn_cvt_pk_fp8_f32(h0[2], h0[3], w0, true); w1 = __builtin_amdgcn_cvt_pk_fp8_f32(h1[0], h1[1], w1, false); w1 = __builtin_amdgcn_cvt_pk_fp8_f32(h1[2], h1[3], w1, true);
;                 *(u32x2*)(hb + (ai * 4 + m) * 512) = (u32x2){w0, w1}; asm volatile("" ::: "memory"); }
	v_add_f32_e32 v18, v22, v23
	v_fmamk_f32 v18, v18, 0x3a800000, v227
	v_rsq_f32_e32 v18, v18
	global_store_dwordx2 v[24:25], v[16:17], off offset:1536 nt
	v_mul_f32_e32 v17, 0x3c800000, v18
	v_mul_f32_e32 v16, 0x3fb8aa3b, v17
	v_pk_mul_f32 v[18:19], v[96:97], v[16:17] op_sel_hi:[1,0]
	v_mul_f32_e32 v20, 0x3f317218, v17
	v_exp_f32_e64 v21, -v18
	v_exp_f32_e64 v17, -v19
	v_pk_mul_f32 v[22:23], v[88:89], v[20:21] op_sel_hi:[1,0]
	v_add_f32_e32 v17, 1.0, v17
	v_pk_mul_f32 v[18:19], v[18:19], v[22:23]
	v_pk_mul_f32 v[22:23], v[98:99], v[16:17] op_sel_hi:[1,0]
	v_add_f32_e32 v21, 1.0, v21
	v_rcp_f32_e32 v29, v17
	v_exp_f32_e64 v17, -v22
	v_rcp_f32_e32 v28, v21
	v_exp_f32_e64 v21, -v23
	v_add_f32_e32 v17, 1.0, v17
	v_pk_mul_f32 v[18:19], v[18:19], v[28:29]
	v_pk_mul_f32 v[28:29], v[90:91], v[20:21] op_sel_hi:[1,0]
	v_rcp_f32_e32 v30, v17
	v_add_f32_e32 v17, 1.0, v21
	v_pk_mul_f32 v[22:23], v[22:23], v[28:29]
	v_pk_mul_f32 v[28:29], v[92:93], v[16:17] op_sel_hi:[1,0]
	v_rcp_f32_e32 v31, v17
	v_exp_f32_e64 v21, -v29
	v_exp_f32_e64 v17, -v28
	v_pk_mul_f32 v[22:23], v[22:23], v[30:31]
	v_pk_mul_f32 v[30:31], v[84:85], v[20:21] op_sel_hi:[1,0]
	v_add_f32_e32 v17, 1.0, v17
	v_pk_mul_f32 v[28:29], v[28:29], v[30:31]
	s_waitcnt vmcnt(6)
	v_mov_b32_e32 v30, v13
	v_mov_b32_e32 v31, v14
	v_mov_b32_e32 v13, v15
	v_pk_add_f32 v[12:13], v[30:31], v[12:13]
	v_rcp_f32_e32 v32, v17
	v_add_f32_e32 v30, v12, v13
	ds_bpermute_b32 v31, v27, v30
	v_add_f32_e32 v17, 1.0, v21
	v_rcp_f32_e32 v33, v17
	v_pk_mul_f32 v[16:17], v[94:95], v[16:17] op_sel_hi:[1,0]
	v_pk_mul_f32 v[20:21], v[86:87], v[20:21] op_sel_hi:[1,0]
	v_exp_f32_e64 v34, -v16
	v_pk_mul_f32 v[14:15], v[16:17], v[20:21]
	s_waitcnt lgkmcnt(0)
	v_add_f32_e32 v20, v30, v31
	ds_bpermute_b32 v21, v26, v20
	v_pk_mul_f32 v[28:29], v[28:29], v[32:33]
	v_exp_f32_e64 v33, -v17
	v_mov_b32_e32 v16, v3
	v_add_f32_e32 v32, 1.0, v34
	v_cvt_pk_fp8_f32 v16, v18, v19
	v_add_f32_e32 v13, 1.0, v33
	s_waitcnt lgkmcnt(0)
	v_add_f32_e32 v18, v20, v21
	v_rcp_f32_e32 v12, v32
	v_rcp_f32_e32 v13, v13
	v_mov_b32_e32 v17, v3
	v_fmamk_f32 v18, v18, 0x3a800000, v227
	v_cvt_pk_fp8_f32 v17, v28, v29
	v_rsq_f32_e32 v18, v18
	v_pk_mul_f32 v[12:13], v[14:15], v[12:13]
	v_cvt_pk_fp8_f32 v16, v22, v23 op_sel:[0,0,1]
	v_cvt_pk_fp8_f32 v17, v12, v13 op_sel:[0,0,1]
	v_mul_f32_e32 v13, 0x3c800000, v18
	v_mul_f32_e32 v12, 0x3fb8aa3b, v13
	v_pk_mul_f32 v[14:15], v[80:81], v[12:13] op_sel_hi:[1,0]
	v_mul_f32_e32 v18, 0x3f317218, v13
	v_exp_f32_e64 v19, -v14
	v_exp_f32_e64 v13, -v15
	global_store_dwordx2 v[24:25], v[16:17], off offset:2048 nt
	v_pk_mul_f32 v[20:21], v[72:73], v[18:19] op_sel_hi:[1,0]
	v_add_f32_e32 v13, 1.0, v13
	v_pk_mul_f32 v[14:15], v[14:15], v[20:21]
	v_pk_mul_f32 v[20:21], v[82:83], v[12:13] op_sel_hi:[1,0]
	v_add_f32_e32 v19, 1.0, v19
	v_rcp_f32_e32 v23, v13
	v_exp_f32_e64 v13, -v20
	v_rcp_f32_e32 v22, v19
	v_exp_f32_e64 v19, -v21
	v_add_f32_e32 v13, 1.0, v13
	v_pk_mul_f32 v[14:15], v[14:15], v[22:23]
	v_pk_mul_f32 v[22:23], v[74:75], v[18:19] op_sel_hi:[1,0]
	v_rcp_f32_e32 v28, v13
	v_add_f32_e32 v13, 1.0, v19
	v_pk_mul_f32 v[20:21], v[20:21], v[22:23]
	v_pk_mul_f32 v[22:23], v[76:77], v[12:13] op_sel_hi:[1,0]
	v_rcp_f32_e32 v29, v13
	v_exp_f32_e64 v13, -v22
	v_exp_f32_e64 v19, -v23
	v_pk_mul_f32 v[20:21], v[20:21], v[28:29]
	v_add_f32_e32 v13, 1.0, v13
	v_rcp_f32_e32 v30, v13
	v_add_f32_e32 v13, 1.0, v19
	v_rcp_f32_e32 v31, v13
	v_pk_mul_f32 v[28:29], v[68:69], v[18:19] op_sel_hi:[1,0]
	v_pk_mul_f32 v[12:13], v[78:79], v[12:13] op_sel_hi:[1,0]
	v_pk_mul_f32 v[22:23], v[22:23], v[28:29]
	v_exp_f32_e64 v28, -v12
	v_pk_mul_f32 v[22:23], v[22:23], v[30:31]
	s_waitcnt vmcnt(6)
	v_mov_b32_e32 v30, v9
	v_mov_b32_e32 v31, v10
	v_mov_b32_e32 v9, v11
	v_pk_add_f32 v[8:9], v[30:31], v[8:9]
	v_exp_f32_e64 v29, -v13
	v_add_f32_e32 v10, v8, v9
	ds_bpermute_b32 v11, v27, v10
	v_mov_b32_e32 v8, v3
	v_add_f32_e32 v28, 1.0, v28
	v_add_f32_e32 v29, 1.0, v29
	v_cvt_pk_fp8_f32 v8, v14, v15
	s_waitcnt lgkmcnt(0)
	v_add_f32_e32 v14, v10, v11
	v_rcp_f32_e32 v28, v28
	v_rcp_f32_e32 v29, v29
	v_mov_b32_e32 v9, v3
	ds_bpermute_b32 v15, v26, v14
	v_cvt_pk_fp8_f32 v9, v22, v23
	v_pk_mul_f32 v[18:19], v[70:71], v[18:19] op_sel_hi:[1,0]
	v_cvt_pk_fp8_f32 v8, v20, v21 op_sel:[0,0,1]
	v_pk_mul_f32 v[10:11], v[12:13], v[18:19]
	s_nop 0
	v_pk_mul_f32 v[10:11], v[10:11], v[28:29]
	s_nop 0
	v_cvt_pk_fp8_f32 v9, v10, v11 op_sel:[0,0,1]
	s_waitcnt lgkmcnt(0)
; __device__ __forceinline__ float rstd_fin4(const f32x4 a) { float s = (a[0] + a[1]) + (a[2] + a[3]); s += __shfl_xor(s, 16); s += __shfl_xor(s, 32); return __builtin_amdgcn_rsqf(s * (1.f / 1024.f) + 1e-6f); }
;     __device__ __forceinline__ void operator()(const f32x4 (&acc)[2][2][4][2], const Unit& u, int wr, int wc, int fr, int fq) const {
;     ...
;             for (int m = 0; m < 4; ++m) { const float rs = rstd_fin4(pa[ai][m]) * sc;
;                 const float rsl = rs * 1.4426950408889634f, rsu = rs * 0.6931471805599453f;
;                 f32x4 h0, h1;
; #pragma unroll
;                 for (int n = 0; n < 2; ++n) { const f32x4 G = acc[ai][0][m][n], U = acc[ai][1][m][n]; f32x4 hv;
; #pragma unroll
;                     for (int q = 0; q < 2; ++q) { const f32x2 g2 = (f32x2){G[2 * q], G[2 * q + 1]} * rsl, u2 = (f32x2){U[2 * q], U[2 * q + 1]} * rsu;
;                         f32x2 r2; r2.x = __builtin_amdgcn_rcpf(1.f + __builtin_amdgcn_exp2f(-g2.x)); r2.y = __builtin_amdgcn_rcpf(1.f + __builtin_amdgcn_exp2f(-g2.y));
;                         const f32x2 o2 = g2 * u2 * r2; hv[2 * q] = o2.x; hv[2 * q + 1] = o2.y; }
;                     if (n == 0) h0 = hv; else h1 = hv; }
;                 unsigned w0 = 0u, w1 = 0u;
;                 w0 = __builtin_amdgcn_cvt_pk_fp8_f32(h0[0], h0[1], w0, false); w0 = __builtin_amdgcn_cvt_pk_fp8_f32(h0[2], h0[3], w0, true); w1 = __builtin_amdgcn_cvt_pk_fp8_f32(h1[0], h1[1], w1, false); w1 = __builtin_amdgcn_cvt_pk_fp8_f32(h1[2], h1[3], w1, true);
;                 *(u32x2*)(hb + (ai * 4 + m) * 512) = (u32x2){w0, w1}; asm volatile("" ::: "memory"); }
	v_add_f32_e32 v10, v14, v15
	v_fmamk_f32 v10, v10, 0x3a800000, v227
	v_rsq_f32_e32 v10, v10
	global_store_dwordx2 v[24:25], v[8:9], off offset:2560 nt
	v_mul_f32_e32 v9, 0x3c800000, v10
	v_mul_f32_e32 v8, 0x3fb8aa3b, v9
	v_pk_mul_f32 v[10:11], v[64:65], v[8:9] op_sel_hi:[1,0]
	v_mul_f32_e32 v12, 0x3f317218, v9
	v_exp_f32_e64 v13, -v10
	v_exp_f32_e64 v9, -v11
	v_pk_mul_f32 v[14:15], v[56:57], v[12:13] op_sel_hi:[1,0]
	v_add_f32_e32 v9, 1.0, v9
	v_pk_mul_f32 v[10:11], v[10:11], v[14:15]
	v_pk_mul_f32 v[14:15], v[66:67], v[8:9] op_sel_hi:[1,0]
	v_add_f32_e32 v13, 1.0, v13
	v_rcp_f32_e32 v17, v9
	v_exp_f32_e64 v9, -v14
	v_rcp_f32_e32 v16, v13
	v_exp_f32_e64 v13, -v15
	v_add_f32_e32 v9, 1.0, v9
	v_pk_mul_f32 v[10:11], v[10:11], v[16:17]
	v_pk_mul_f32 v[16:17], v[58:59], v[12:13] op_sel_hi:[1,0]
	v_rcp_f32_e32 v18, v9
	v_add_f32_e32 v9, 1.0, v13
	v_pk_mul_f32 v[14:15], v[14:15], v[16:17]
	v_pk_mul_f32 v[16:17], v[60:61], v[8:9] op_sel_hi:[1,0]
	v_rcp_f32_e32 v19, v9
	v_exp_f32_e64 v13, -v17
	v_exp_f32_e64 v9, -v16
	v_pk_mul_f32 v[14:15], v[14:15], v[18:19]
	v_pk_mul_f32 v[18:19], v[52:53], v[12:13] op_sel_hi:[1,0]
	v_add_f32_e32 v9, 1.0, v9
	v_pk_mul_f32 v[16:17], v[16:17], v[18:19]
	s_waitcnt vmcnt(6)
	v_mov_b32_e32 v18, v5
	v_mov_b32_e32 v19, v6
	v_mov_b32_e32 v5, v7
	v_pk_add_f32 v[4:5], v[18:19], v[4:5]
	v_rcp_f32_e32 v20, v9
	v_add_f32_e32 v18, v4, v5
	ds_bpermute_b32 v19, v27, v18
	v_add_f32_e32 v9, 1.0, v13
	v_rcp_f32_e32 v21, v9
	v_pk_mul_f32 v[8:9], v[62:63], v[8:9] op_sel_hi:[1,0]
	v_pk_mul_f32 v[12:13], v[54:55], v[12:13] op_sel_hi:[1,0]
	v_exp_f32_e64 v22, -v8
	v_pk_mul_f32 v[6:7], v[8:9], v[12:13]
	s_waitcnt lgkmcnt(0)
	v_add_f32_e32 v12, v18, v19
	ds_bpermute_b32 v13, v26, v12
	v_pk_mul_f32 v[16:17], v[16:17], v[20:21]
	v_exp_f32_e64 v21, -v9
	v_mov_b32_e32 v8, v3
	v_add_f32_e32 v20, 1.0, v22
	v_cvt_pk_fp8_f32 v8, v10, v11
	v_add_f32_e32 v5, 1.0, v21
	s_waitcnt lgkmcnt(0)
	v_add_f32_e32 v10, v12, v13
	v_rcp_f32_e32 v4, v20
	v_rcp_f32_e32 v5, v5
	v_mov_b32_e32 v9, v3
	v_fmamk_f32 v10, v10, 0x3a800000, v227
	v_cvt_pk_fp8_f32 v9, v16, v17
	v_rsq_f32_e32 v10, v10
	v_pk_mul_f32 v[4:5], v[6:7], v[4:5]
	v_cvt_pk_fp8_f32 v8, v14, v15 op_sel:[0,0,1]
	v_cvt_pk_fp8_f32 v9, v4, v5 op_sel:[0,0,1]
	v_mul_f32_e32 v5, 0x3c800000, v10
	v_mul_f32_e32 v4, 0x3fb8aa3b, v5
	v_pk_mul_f32 v[6:7], v[48:49], v[4:5] op_sel_hi:[1,0]
	v_mul_f32_e32 v10, 0x3f317218, v5
	v_exp_f32_e64 v11, -v6
	v_exp_f32_e64 v5, -v7
	global_store_dwordx2 v[24:25], v[8:9], off offset:3072 nt
	v_pk_mul_f32 v[12:13], v[40:41], v[10:11] op_sel_hi:[1,0]
	v_add_f32_e32 v5, 1.0, v5
	v_pk_mul_f32 v[6:7], v[6:7], v[12:13]
	v_pk_mul_f32 v[12:13], v[50:51], v[4:5] op_sel_hi:[1,0]
	v_add_f32_e32 v11, 1.0, v11
	v_rcp_f32_e32 v15, v5
	v_exp_f32_e64 v5, -v12
	v_rcp_f32_e32 v14, v11
	v_exp_f32_e64 v11, -v13
	v_add_f32_e32 v5, 1.0, v5
	v_pk_mul_f32 v[6:7], v[6:7], v[14:15]
	v_pk_mul_f32 v[14:15], v[42:43], v[10:11] op_sel_hi:[1,0]
	v_rcp_f32_e32 v16, v5
	v_add_f32_e32 v5, 1.0, v11
	v_pk_mul_f32 v[12:13], v[12:13], v[14:15]
	v_pk_mul_f32 v[14:15], v[44:45], v[4:5] op_sel_hi:[1,0]
	v_rcp_f32_e32 v17, v5
	v_exp_f32_e64 v5, -v14
	v_exp_f32_e64 v11, -v15
	v_pk_mul_f32 v[12:13], v[12:13], v[16:17]
	v_add_f32_e32 v5, 1.0, v5
	v_rcp_f32_e32 v18, v5
	v_add_f32_e32 v5, 1.0, v11
	v_pk_mul_f32 v[16:17], v[36:37], v[10:11] op_sel_hi:[1,0]
	v_rcp_f32_e32 v19, v5
	v_pk_mul_f32 v[4:5], v[46:47], v[4:5] op_sel_hi:[1,0]
	v_pk_mul_f32 v[14:15], v[14:15], v[16:17]
	v_exp_f32_e64 v16, -v4
	v_exp_f32_e64 v17, -v5
	v_pk_mul_f32 v[14:15], v[14:15], v[18:19]
	v_mov_b32_e32 v18, v3
	v_add_f32_e32 v16, 1.0, v16
	v_add_f32_e32 v17, 1.0, v17
	v_rcp_f32_e32 v16, v16
	v_rcp_f32_e32 v17, v17
	v_mov_b32_e32 v19, v3
	v_cvt_pk_fp8_f32 v18, v6, v7
	v_cvt_pk_fp8_f32 v19, v14, v15
	v_pk_mul_f32 v[10:11], v[38:39], v[10:11] op_sel_hi:[1,0]
	v_cvt_pk_fp8_f32 v18, v12, v13 op_sel:[0,0,1]
	v_pk_mul_f32 v[4:5], v[4:5], v[10:11]
	s_nop 0
	v_pk_mul_f32 v[4:5], v[4:5], v[16:17]
	s_nop 0
	v_cvt_pk_fp8_f32 v19, v4, v5 op_sel:[0,0,1]
	global_store_dwordx2 v[24:25], v[18:19], off offset:3584 nt
	s_cbranch_vccnz .LBB0_1685
	s_andn2_b64 vcc, exec, s[38:39]
	s_cbranch_vccnz .LBB0_1684
	s_barrier
	s_branch .LBB0_1684

; __device__ __forceinline__ float rstd_fin4(const f32x4 a) { float s = (a[0] + a[1]) + (a[2] + a[3]); s += __shfl_xor(s, 16); s += __shfl_xor(s, 32); return __builtin_amdgcn_rsqf(s * (1.f / 1024.f) + 1e-6f); }
;     __device__ __forceinline__ void operator()(const f32x4 (&acc)[2][2][4][2], const Unit& u, int wr, int wc, int fr, int fq) const {
;     ...
;         const int row0 = u.pm * BM + wr * 64 + fr;
;         unsigned char* const hb = (unsigned char*)H + (size_t)(u.pm * (FFH / 128) + u.pn + pn0) * 32768 + (((wr * 4 + wc) * 8) * 64 + (fq >> 1) * 32 + fr * 2 + (fq & 1)) * 8;
;         f32x4 pa[2][4];
; #pragma unroll
;         for (int ai = 0; ai < 2; ++ai)
; #pragma unroll
;             for (int m = 0; m < 4; ++m) pa[ai][m] = rstd_ld4(ss, row0 + ai * HALF + m * 16, fq);
; #pragma unroll
;         for (int ai = 0; ai < 2; ++ai)
; #pragma unroll
;             for (int m = 0; m < 4; ++m) { const float rs = rstd_fin4(pa[ai][m]) * sc;
;                 const float rsl = rs * 1.4426950408889634f, rsu = rs * 0.6931471805599453f;
;                 f32x4 h0, h1;
; #pragma unroll
;                 for (int n = 0; n < 2; ++n) { const f32x4 G = acc[ai][0][m][n], U = acc[ai][1][m][n]; f32x4 hv;
; #pragma unroll
;                     for (int q = 0; q < 2; ++q) { const f32x2 g2 = (f32x2){G[2 * q], G[2 * q + 1]} * rsl, u2 = (f32x2){U[2 * q], U[2 * q + 1]} * rsu;
;                         f32x2 r2; r2.x = __builtin_amdgcn_rcpf(1.f + __builtin_amdgcn_exp2f(-g2.x)); r2.y = __builtin_amdgcn_rcpf(1.f + __builtin_amdgcn_exp2f(-g2.y));
.LBB0_1712:
	s_lshl_b32 s4, s70, 8
	v_mov_b32_e32 v142, v168
	v_mov_b32_e32 v143, v1
	s_add_i32 s4, s4, s64
	v_and_b32_e32 v145, 64, v246
	v_add_u32_e32 v124, s4, v143
	v_lshlrev_b32_e32 v126, 2, v142
	v_ashrrev_i32_e32 v127, 31, v126
	v_ashrrev_i32_e32 v125, 31, v124
	v_lshl_add_u64 v[126:127], v[126:127], 2, s[44:45]
	v_lshlrev_b64 v[124:125], 6, v[124:125]
	v_lshl_add_u64 v[140:141], v[126:127], 0, v[124:125]
	global_load_dwordx4 v[136:139], v[140:141], off
	global_load_dwordx4 v[124:127], v[140:141], off offset:1024
	global_load_dwordx4 v[152:155], v[140:141], off offset:2048
	global_load_dwordx4 v[148:151], v[140:141], off offset:3072
	v_xor_b32_e32 v144, 16, v246
	v_add_u32_e32 v145, 64, v145
	v_xor_b32_e32 v146, 32, v246
	v_cmp_lt_i32_e32 vcc, v144, v145
	v_mov_b32_e32 v174, v3
	v_mov_b32_e32 v175, v3
	v_cndmask_b32_e32 v144, v246, v144, vcc
	v_cmp_lt_i32_e32 vcc, v146, v145
	v_lshlrev_b32_e32 v172, 2, v144
	s_mul_i32 s4, s70, 22
	v_cndmask_b32_e32 v145, v246, v146, vcc
	v_lshlrev_b32_e32 v171, 2, v145
	s_add_i32 s4, s69, s4
	s_add_i32 s4, s4, 18
	v_lshlrev_b32_e32 v147, 4, v142
	v_lshl_add_u32 v143, v143, 1, s67
	s_ashr_i32 s5, s4, 31
	v_and_b32_e32 v146, 0x1fffffe0, v147
	v_and_or_b32 v142, v142, 1, v143
	s_lshl_b64 s[4:5], s[4:5], 15
	v_add_lshl_u32 v142, v142, v146, 3
	s_add_u32 s4, s6, s4
	v_ashrrev_i32_e32 v143, 31, v142
	s_addc_u32 s5, s7, s5
	v_lshl_add_u64 v[166:167], s[4:5], 0, v[142:143]
	s_mov_b64 s[4:5], -1
	s_waitcnt vmcnt(0)
	v_mov_b32_e32 v144, v137
	v_mov_b32_e32 v145, v138
	v_mov_b32_e32 v137, v139
	v_mov_b32_e32 v138, v125
	v_mov_b32_e32 v139, v126
	v_mov_b32_e32 v125, v127
	v_pk_add_f32 v[126:127], v[144:145], v[136:137]
	v_pk_add_f32 v[124:125], v[138:139], v[124:125]
	v_add_f32_e32 v126, v126, v127
	v_add_f32_e32 v127, v124, v125
	ds_bpermute_b32 v136, v172, v126
	ds_bpermute_b32 v137, v172, v127
	v_add_co_u32_e32 v124, vcc, s88, v140
	s_waitcnt lgkmcnt(1)
	v_add_f32_e32 v126, v126, v136
	s_waitcnt lgkmcnt(0)
	v_add_f32_e32 v127, v127, v137
	ds_bpermute_b32 v136, v171, v126
	ds_bpermute_b32 v137, v171, v127
	v_addc_co_u32_e32 v125, vcc, 0, v141, vcc
	global_load_dwordx4 v[144:147], v[124:125], off
	global_load_dwordx4 v[140:143], v[124:125], off offset:1024
	s_waitcnt lgkmcnt(1)
	v_add_f32_e32 v126, v126, v136
	s_waitcnt lgkmcnt(0)
	v_add_f32_e32 v127, v127, v137
	v_fmamk_f32 v126, v126, 0x3a800000, v227
	v_fmamk_f32 v127, v127, 0x3a800000, v227
	v_rsq_f32_e32 v173, v126
	v_rsq_f32_e32 v177, v127
	global_load_dwordx4 v[136:139], v[124:125], off offset:2048
	s_nop 0
	global_load_dwordx4 v[124:127], v[124:125], off offset:3072
	s_andn2_b64 vcc, exec, s[40:41]
	v_mul_f32_e32 v176, 0x3fb8aa3b, v173
	v_mul_f32_e32 v178, 0x3f317218, v173
	v_pk_mul_f32 v[132:133], v[132:133], v[176:177] op_sel_hi:[1,0]
	v_pk_mul_f32 v[120:121], v[120:121], v[178:179] op_sel_hi:[1,0]
	v_pk_mul_f32 v[134:135], v[134:135], v[176:177] op_sel_hi:[1,0]
	v_pk_mul_f32 v[122:123], v[122:123], v[178:179] op_sel_hi:[1,0]
	v_pk_mul_f32 v[128:129], v[128:129], v[176:177] op_sel_hi:[1,0]
	v_pk_mul_f32 v[116:117], v[116:117], v[178:179] op_sel_hi:[1,0]
	v_pk_mul_f32 v[130:131], v[130:131], v[176:177] op_sel_hi:[1,0]
	v_exp_f32_e64 v173, -v132
	v_exp_f32_e64 v176, -v133
	v_pk_mul_f32 v[120:121], v[132:133], v[120:121]
	v_exp_f32_e64 v132, -v134
	v_exp_f32_e64 v133, -v135
	v_pk_mul_f32 v[122:123], v[134:135], v[122:123]
	v_exp_f32_e64 v134, -v128
	v_exp_f32_e64 v135, -v129
	v_pk_mul_f32 v[116:117], v[128:129], v[116:117]
	v_exp_f32_e64 v128, -v130
	v_exp_f32_e64 v129, -v131
	v_pk_mul_f32 v[118:119], v[118:119], v[178:179] op_sel_hi:[1,0]
	v_add_f32_e32 v132, 1.0, v132
	v_pk_mul_f32 v[118:119], v[130:131], v[118:119]
	v_add_f32_e32 v130, 1.0, v173
	v_add_f32_e32 v131, 1.0, v176
	v_add_f32_e32 v173, 1.0, v128
	v_add_f32_e32 v176, 1.0, v129
	v_rcp_f32_e32 v128, v130
	v_rcp_f32_e32 v129, v131
	v_add_f32_e32 v133, 1.0, v133
	v_add_f32_e32 v134, 1.0, v134
	v_add_f32_e32 v135, 1.0, v135
	v_rcp_f32_e32 v130, v132
	v_rcp_f32_e32 v131, v133
	v_rcp_f32_e32 v132, v134
	v_rcp_f32_e32 v133, v135
	v_pk_mul_f32 v[120:121], v[120:121], v[128:129]
	v_mul_f32_e32 v180, 0x3fb8aa3b, v177
	v_cvt_pk_fp8_f32 v174, v120, v121
	v_mul_f32_e32 v182, 0x3f317218, v177
	v_pk_mul_f32 v[116:117], v[116:117], v[132:133]
	v_pk_mul_f32 v[112:113], v[112:113], v[180:181] op_sel_hi:[1,0]
	v_pk_mul_f32 v[108:109], v[108:109], v[182:183] op_sel_hi:[1,0]
	v_cvt_pk_fp8_f32 v175, v116, v117
	v_pk_mul_f32 v[116:117], v[122:123], v[130:131]
	v_exp_f32_e64 v177, -v112
	v_cvt_pk_fp8_f32 v174, v116, v117 op_sel:[0,0,1]
	v_exp_f32_e64 v117, -v113
	v_pk_mul_f32 v[108:109], v[112:113], v[108:109]
	v_pk_mul_f32 v[112:113], v[114:115], v[180:181] op_sel_hi:[1,0]
	v_pk_mul_f32 v[110:111], v[110:111], v[182:183] op_sel_hi:[1,0]
	v_exp_f32_e64 v114, -v112
	v_exp_f32_e64 v115, -v113
	v_pk_mul_f32 v[104:105], v[104:105], v[180:181] op_sel_hi:[1,0]
	v_pk_mul_f32 v[110:111], v[112:113], v[110:111]
	v_add_f32_e32 v114, 1.0, v114
	v_add_f32_e32 v115, 1.0, v115
	v_exp_f32_e64 v112, -v104
	v_exp_f32_e64 v113, -v105
	v_rcp_f32_e32 v114, v114
	v_rcp_f32_e32 v115, v115
	v_add_f32_e32 v112, 1.0, v112
	v_add_f32_e32 v113, 1.0, v113
	v_pk_mul_f32 v[106:107], v[106:107], v[180:181] op_sel_hi:[1,0]
	v_pk_mul_f32 v[110:111], v[110:111], v[114:115]
	v_rcp_f32_e32 v112, v112
	v_rcp_f32_e32 v113, v113
	v_exp_f32_e64 v114, -v106
	v_pk_mul_f32 v[100:101], v[100:101], v[182:183] op_sel_hi:[1,0]
	v_add_f32_e32 v116, 1.0, v177
	v_pk_mul_f32 v[100:101], v[104:105], v[100:101]
	v_mov_b32_e32 v104, v153
	v_mov_b32_e32 v105, v154
	v_mov_b32_e32 v153, v155
	v_pk_add_f32 v[104:105], v[104:105], v[152:153]
	v_pk_mul_f32 v[100:101], v[100:101], v[112:113]
	v_add_f32_e32 v112, 1.0, v114
	v_add_f32_e32 v114, v104, v105
	ds_bpermute_b32 v115, v172, v114
	v_exp_f32_e64 v113, -v107
	v_rcp_f32_e32 v104, v112
	v_add_f32_e32 v117, 1.0, v117
	v_rcp_f32_e32 v116, v116
	s_waitcnt lgkmcnt(0)
; __device__ __forceinline__ float rstd_fin4(const f32x4 a) { float s = (a[0] + a[1]) + (a[2] + a[3]); s += __shfl_xor(s, 16); s += __shfl_xor(s, 32); return __builtin_amdgcn_rsqf(s * (1.f / 1024.f) + 1e-6f); }
;     __device__ __forceinline__ void operator()(const f32x4 (&acc)[2][2][4][2], const Unit& u, int wr, int wc, int fr, int fq) const {
;     ...
;             for (int m = 0; m < 4; ++m) { const float rs = rstd_fin4(pa[ai][m]) * sc;
;                 const float rsl = rs * 1.4426950408889634f, rsu = rs * 0.6931471805599453f;
;                 f32x4 h0, h1;
; #pragma unroll
;                 for (int n = 0; n < 2; ++n) { const f32x4 G = acc[ai][0][m][n], U = acc[ai][1][m][n]; f32x4 hv;
; #pragma unroll
;                     for (int q = 0; q < 2; ++q) { const f32x2 g2 = (f32x2){G[2 * q], G[2 * q + 1]} * rsl, u2 = (f32x2){U[2 * q], U[2 * q + 1]} * rsu;
;                         f32x2 r2; r2.x = __builtin_amdgcn_rcpf(1.f + __builtin_amdgcn_exp2f(-g2.x)); r2.y = __builtin_amdgcn_rcpf(1.f + __builtin_amdgcn_exp2f(-g2.y));
;                         const f32x2 o2 = g2 * u2 * r2; hv[2 * q] = o2.x; hv[2 * q + 1] = o2.y; }
;                     if (n == 0) h0 = hv; else h1 = hv; }
;                 unsigned w0 = 0u, w1 = 0u;
;                 w0 = __builtin_amdgcn_cvt_pk_fp8_f32(h0[0], h0[1], w0, false); w0 = __builtin_amdgcn_cvt_pk_fp8_f32(h0[2], h0[3], w0, true); w1 = __builtin_amdgcn_cvt_pk_fp8_f32(h1[0], h1[1], w1, false); w1 = __builtin_amdgcn_cvt_pk_fp8_f32(h1[2], h1[3], w1, true);
;                 *(u32x2*)(hb + (ai * 4 + m) * 512) = (u32x2){w0, w1}; asm volatile("" ::: "memory"); }
	v_add_f32_e32 v112, v114, v115
	v_add_f32_e32 v105, 1.0, v113
	ds_bpermute_b32 v113, v171, v112
	v_rcp_f32_e32 v117, v117
	v_pk_mul_f32 v[102:103], v[102:103], v[182:183] op_sel_hi:[1,0]
	v_rcp_f32_e32 v105, v105
	v_pk_mul_f32 v[102:103], v[106:107], v[102:103]
	v_mov_b32_e32 v107, v3
	v_cvt_pk_fp8_f32 v107, v100, v101
	s_waitcnt lgkmcnt(0)
	v_add_f32_e32 v100, v112, v113
	v_pk_mul_f32 v[108:109], v[108:109], v[116:117]
	v_mov_b32_e32 v106, v3
	v_fmamk_f32 v100, v100, 0x3a800000, v227
	v_cvt_pk_fp8_f32 v106, v108, v109
	v_rsq_f32_e32 v108, v100
	v_pk_mul_f32 v[100:101], v[102:103], v[104:105]
	v_rcp_f32_e32 v134, v173
	v_cvt_pk_fp8_f32 v107, v100, v101 op_sel:[0,0,1]
	v_mul_f32_e32 v100, 0x3fb8aa3b, v108
	v_pk_mul_f32 v[96:97], v[96:97], v[100:101] op_sel_hi:[1,0]
	v_mul_f32_e32 v102, 0x3f317218, v108
	v_exp_f32_e64 v101, -v96
	v_exp_f32_e64 v103, -v97
	v_rcp_f32_e32 v135, v176
	v_cvt_pk_fp8_f32 v106, v110, v111 op_sel:[0,0,1]
	v_add_f32_e32 v101, 1.0, v101
	v_pk_mul_f32 v[92:93], v[92:93], v[102:103] op_sel_hi:[1,0]
	v_rcp_f32_e32 v104, v101
	v_add_f32_e32 v101, 1.0, v103
	v_pk_mul_f32 v[92:93], v[96:97], v[92:93]
	v_pk_mul_f32 v[96:97], v[98:99], v[100:101] op_sel_hi:[1,0]
	v_pk_mul_f32 v[94:95], v[94:95], v[102:103] op_sel_hi:[1,0]
	v_pk_mul_f32 v[88:89], v[88:89], v[100:101] op_sel_hi:[1,0]
	v_exp_f32_e64 v98, -v96
	v_exp_f32_e64 v99, -v97
	v_pk_mul_f32 v[94:95], v[96:97], v[94:95]
	v_exp_f32_e64 v96, -v88
	v_exp_f32_e64 v97, -v89
	v_add_f32_e32 v98, 1.0, v98
	v_add_f32_e32 v99, 1.0, v99
	v_add_f32_e32 v96, 1.0, v96
	v_add_f32_e32 v97, 1.0, v97
	v_rcp_f32_e32 v96, v96
	v_rcp_f32_e32 v97, v97
	v_rcp_f32_e32 v98, v98
	v_rcp_f32_e32 v99, v99
	v_pk_mul_f32 v[84:85], v[84:85], v[102:103] op_sel_hi:[1,0]
	v_rcp_f32_e32 v105, v101
	v_pk_mul_f32 v[84:85], v[88:89], v[84:85]
	v_pk_mul_f32 v[94:95], v[94:95], v[98:99]
	v_pk_mul_f32 v[84:85], v[84:85], v[96:97]
	v_mov_b32_e32 v96, v149
	v_mov_b32_e32 v97, v150
	v_mov_b32_e32 v149, v151
	v_pk_add_f32 v[96:97], v[96:97], v[148:149]
	v_pk_mul_f32 v[88:89], v[90:91], v[100:101] op_sel_hi:[1,0]
	v_add_f32_e32 v98, v96, v97
	ds_bpermute_b32 v99, v172, v98
	v_exp_f32_e64 v90, -v88
	v_exp_f32_e64 v91, -v89
	v_pk_mul_f32 v[92:93], v[92:93], v[104:105]
	v_mov_b32_e32 v96, v3
	v_add_f32_e32 v90, 1.0, v90
	v_add_f32_e32 v91, 1.0, v91
	v_cvt_pk_fp8_f32 v96, v92, v93
	s_waitcnt lgkmcnt(0)
	v_add_f32_e32 v92, v98, v99
	v_rcp_f32_e32 v90, v90
	v_rcp_f32_e32 v91, v91
	v_mov_b32_e32 v97, v3
	ds_bpermute_b32 v93, v171, v92
	v_cvt_pk_fp8_f32 v97, v84, v85
	v_pk_mul_f32 v[86:87], v[86:87], v[102:103] op_sel_hi:[1,0]
	v_pk_mul_f32 v[118:119], v[118:119], v[134:135]
	v_pk_mul_f32 v[84:85], v[88:89], v[86:87]
	v_cvt_pk_fp8_f32 v175, v118, v119 op_sel:[0,0,1]
	v_pk_mul_f32 v[84:85], v[84:85], v[90:91]
	v_cvt_pk_fp8_f32 v96, v94, v95 op_sel:[0,0,1]
	v_cvt_pk_fp8_f32 v97, v84, v85 op_sel:[0,0,1]
	s_waitcnt lgkmcnt(0)
	v_add_f32_e32 v84, v92, v93
	v_fmamk_f32 v84, v84, 0x3a800000, v227
	v_rsq_f32_e32 v85, v84
	global_store_dwordx2 v[166:167], v[174:175], off nt
	global_store_dwordx2 v[166:167], v[106:107], off offset:512 nt
	v_mul_f32_e32 v84, 0x3fb8aa3b, v85
	v_pk_mul_f32 v[80:81], v[80:81], v[84:85] op_sel_hi:[1,0]
	v_mul_f32_e32 v86, 0x3f317218, v85
	v_exp_f32_e64 v87, -v80
	v_exp_f32_e64 v85, -v81
	global_store_dwordx2 v[166:167], v[96:97], off offset:1024 nt
	v_pk_mul_f32 v[76:77], v[76:77], v[86:87] op_sel_hi:[1,0]
	v_add_f32_e32 v87, 1.0, v87
	v_add_f32_e32 v85, 1.0, v85
	v_pk_mul_f32 v[76:77], v[80:81], v[76:77]
	v_pk_mul_f32 v[80:81], v[82:83], v[84:85] op_sel_hi:[1,0]
	v_pk_mul_f32 v[78:79], v[78:79], v[86:87] op_sel_hi:[1,0]
	v_pk_mul_f32 v[72:73], v[72:73], v[84:85] op_sel_hi:[1,0]
	v_exp_f32_e64 v82, -v80
	v_exp_f32_e64 v83, -v81
	v_pk_mul_f32 v[78:79], v[80:81], v[78:79]
	v_exp_f32_e64 v80, -v72
	v_exp_f32_e64 v81, -v73
	v_add_f32_e32 v82, 1.0, v82
	v_add_f32_e32 v83, 1.0, v83
	v_add_f32_e32 v80, 1.0, v80
	v_add_f32_e32 v81, 1.0, v81
	v_rcp_f32_e32 v80, v80
	v_rcp_f32_e32 v81, v81
	v_rcp_f32_e32 v82, v82
	v_rcp_f32_e32 v83, v83
	v_pk_mul_f32 v[68:69], v[68:69], v[86:87] op_sel_hi:[1,0]
	v_rcp_f32_e32 v88, v87
	v_pk_mul_f32 v[68:69], v[72:73], v[68:69]
	v_pk_mul_f32 v[78:79], v[78:79], v[82:83]
	v_pk_mul_f32 v[68:69], v[68:69], v[80:81]
	s_waitcnt vmcnt(6)
	v_mov_b32_e32 v80, v145
	v_mov_b32_e32 v81, v146
	v_mov_b32_e32 v145, v147
	v_pk_add_f32 v[80:81], v[80:81], v[144:145]
	v_rcp_f32_e32 v89, v85
	v_add_f32_e32 v82, v80, v81
	v_pk_mul_f32 v[72:73], v[74:75], v[84:85] op_sel_hi:[1,0]
	ds_bpermute_b32 v83, v172, v82
	v_exp_f32_e64 v74, -v72
	v_exp_f32_e64 v75, -v73
	v_pk_mul_f32 v[76:77], v[76:77], v[88:89]
	v_mov_b32_e32 v80, v3
	v_add_f32_e32 v74, 1.0, v74
	v_add_f32_e32 v75, 1.0, v75
	v_cvt_pk_fp8_f32 v80, v76, v77
	s_waitcnt lgkmcnt(0)
	v_add_f32_e32 v76, v82, v83
	v_rcp_f32_e32 v74, v74
	v_rcp_f32_e32 v75, v75
	v_mov_b32_e32 v81, v3
	ds_bpermute_b32 v77, v171, v76
	v_cvt_pk_fp8_f32 v81, v68, v69
	v_pk_mul_f32 v[70:71], v[70:71], v[86:87] op_sel_hi:[1,0]
	v_cvt_pk_fp8_f32 v80, v78, v79 op_sel:[0,0,1]
	v_pk_mul_f32 v[68:69], v[72:73], v[70:71]
	s_nop 0
	v_pk_mul_f32 v[68:69], v[68:69], v[74:75]
	s_nop 0
	v_cvt_pk_fp8_f32 v81, v68, v69 op_sel:[0,0,1]
	s_waitcnt lgkmcnt(0)
; __device__ __forceinline__ float rstd_fin4(const f32x4 a) { float s = (a[0] + a[1]) + (a[2] + a[3]); s += __shfl_xor(s, 16); s += __shfl_xor(s, 32); return __builtin_amdgcn_rsqf(s * (1.f / 1024.f) + 1e-6f); }
;     __device__ __forceinline__ void operator()(const f32x4 (&acc)[2][2][4][2], const Unit& u, int wr, int wc, int fr, int fq) const {
;     ...
;             for (int m = 0; m < 4; ++m) { const float rs = rstd_fin4(pa[ai][m]) * sc;
;                 const float rsl = rs * 1.4426950408889634f, rsu = rs * 0.6931471805599453f;
;                 f32x4 h0, h1;
; #pragma unroll
;                 for (int n = 0; n < 2; ++n) { const f32x4 G = acc[ai][0][m][n], U = acc[ai][1][m][n]; f32x4 hv;
; #pragma unroll
;                     for (int q = 0; q < 2; ++q) { const f32x2 g2 = (f32x2){G[2 * q], G[2 * q + 1]} * rsl, u2 = (f32x2){U[2 * q], U[2 * q + 1]} * rsu;
;                         f32x2 r2; r2.x = __builtin_amdgcn_rcpf(1.f + __builtin_amdgcn_exp2f(-g2.x)); r2.y = __builtin_amdgcn_rcpf(1.f + __builtin_amdgcn_exp2f(-g2.y));
;                         const f32x2 o2 = g2 * u2 * r2; hv[2 * q] = o2.x; hv[2 * q + 1] = o2.y; }
;                     if (n == 0) h0 = hv; else h1 = hv; }
;                 unsigned w0 = 0u, w1 = 0u;
;                 w0 = __builtin_amdgcn_cvt_pk_fp8_f32(h0[0], h0[1], w0, false); w0 = __builtin_amdgcn_cvt_pk_fp8_f32(h0[2], h0[3], w0, true); w1 = __builtin_amdgcn_cvt_pk_fp8_f32(h1[0], h1[1], w1, false); w1 = __builtin_amdgcn_cvt_pk_fp8_f32(h1[2], h1[3], w1, true);
;                 *(u32x2*)(hb + (ai * 4 + m) * 512) = (u32x2){w0, w1}; asm volatile("" ::: "memory"); }
	v_add_f32_e32 v68, v76, v77
	v_fmamk_f32 v68, v68, 0x3a800000, v227
	v_rsq_f32_e32 v69, v68
	global_store_dwordx2 v[166:167], v[80:81], off offset:1536 nt
	v_mul_f32_e32 v68, 0x3fb8aa3b, v69
	v_pk_mul_f32 v[64:65], v[64:65], v[68:69] op_sel_hi:[1,0]
	v_mul_f32_e32 v70, 0x3f317218, v69
	v_exp_f32_e64 v71, -v64
	v_exp_f32_e64 v69, -v65
	v_pk_mul_f32 v[60:61], v[60:61], v[70:71] op_sel_hi:[1,0]
	v_add_f32_e32 v69, 1.0, v69
	v_pk_mul_f32 v[60:61], v[64:65], v[60:61]
	v_pk_mul_f32 v[64:65], v[66:67], v[68:69] op_sel_hi:[1,0]
	v_add_f32_e32 v71, 1.0, v71
	v_exp_f32_e64 v66, -v64
	v_exp_f32_e64 v67, -v65
	v_pk_mul_f32 v[62:63], v[62:63], v[70:71] op_sel_hi:[1,0]
	v_pk_mul_f32 v[56:57], v[56:57], v[68:69] op_sel_hi:[1,0]
	v_add_f32_e32 v66, 1.0, v66
	v_add_f32_e32 v67, 1.0, v67
	v_pk_mul_f32 v[62:63], v[64:65], v[62:63]
	v_exp_f32_e64 v64, -v56
	v_exp_f32_e64 v65, -v57
	v_rcp_f32_e32 v66, v66
	v_rcp_f32_e32 v67, v67
	v_add_f32_e32 v64, 1.0, v64
	v_add_f32_e32 v65, 1.0, v65
	v_pk_mul_f32 v[58:59], v[58:59], v[68:69] op_sel_hi:[1,0]
	v_pk_mul_f32 v[62:63], v[62:63], v[66:67]
	v_rcp_f32_e32 v64, v64
	v_rcp_f32_e32 v65, v65
	v_exp_f32_e64 v66, -v58
	v_pk_mul_f32 v[52:53], v[52:53], v[70:71] op_sel_hi:[1,0]
	v_rcp_f32_e32 v72, v71
	v_pk_mul_f32 v[52:53], v[56:57], v[52:53]
	s_waitcnt vmcnt(6)
	v_mov_b32_e32 v56, v141
	v_mov_b32_e32 v57, v142
	v_mov_b32_e32 v141, v143
	v_pk_add_f32 v[56:57], v[56:57], v[140:141]
	v_pk_mul_f32 v[52:53], v[52:53], v[64:65]
	v_add_f32_e32 v64, 1.0, v66
	v_add_f32_e32 v66, v56, v57
	ds_bpermute_b32 v67, v172, v66
	v_exp_f32_e64 v65, -v59
	v_rcp_f32_e32 v56, v64
	v_rcp_f32_e32 v73, v69
	v_pk_mul_f32 v[54:55], v[54:55], v[70:71] op_sel_hi:[1,0]
	s_waitcnt lgkmcnt(0)
	v_add_f32_e32 v64, v66, v67
	v_add_f32_e32 v57, 1.0, v65
	ds_bpermute_b32 v65, v171, v64
	v_pk_mul_f32 v[54:55], v[58:59], v[54:55]
	v_mov_b32_e32 v59, v3
	v_cvt_pk_fp8_f32 v59, v52, v53
	v_pk_mul_f32 v[60:61], v[60:61], v[72:73]
	s_waitcnt lgkmcnt(0)
	v_add_f32_e32 v52, v64, v65
	v_rcp_f32_e32 v57, v57
	v_mov_b32_e32 v58, v3
	v_fmamk_f32 v52, v52, 0x3a800000, v227
	v_cvt_pk_fp8_f32 v58, v60, v61
	v_rsq_f32_e32 v60, v52
	v_pk_mul_f32 v[52:53], v[54:55], v[56:57]
	v_cvt_pk_fp8_f32 v58, v62, v63 op_sel:[0,0,1]
	v_cvt_pk_fp8_f32 v59, v52, v53 op_sel:[0,0,1]
	v_mul_f32_e32 v52, 0x3fb8aa3b, v60
	v_pk_mul_f32 v[48:49], v[48:49], v[52:53] op_sel_hi:[1,0]
	v_mul_f32_e32 v54, 0x3f317218, v60
	v_exp_f32_e64 v53, -v48
	v_exp_f32_e64 v55, -v49
	global_store_dwordx2 v[166:167], v[58:59], off offset:2048 nt
	v_add_f32_e32 v53, 1.0, v53
	v_pk_mul_f32 v[44:45], v[44:45], v[54:55] op_sel_hi:[1,0]
	v_rcp_f32_e32 v56, v53
	v_add_f32_e32 v53, 1.0, v55
	v_pk_mul_f32 v[44:45], v[48:49], v[44:45]
	v_pk_mul_f32 v[48:49], v[50:51], v[52:53] op_sel_hi:[1,0]
	v_pk_mul_f32 v[46:47], v[46:47], v[54:55] op_sel_hi:[1,0]
	v_pk_mul_f32 v[40:41], v[40:41], v[52:53] op_sel_hi:[1,0]
	v_exp_f32_e64 v50, -v48
	v_exp_f32_e64 v51, -v49
	v_pk_mul_f32 v[46:47], v[48:49], v[46:47]
	v_exp_f32_e64 v48, -v40
	v_exp_f32_e64 v49, -v41
	v_add_f32_e32 v50, 1.0, v50
	v_add_f32_e32 v51, 1.0, v51
	v_add_f32_e32 v48, 1.0, v48
	v_add_f32_e32 v49, 1.0, v49
	v_rcp_f32_e32 v48, v48
	v_rcp_f32_e32 v49, v49
	v_rcp_f32_e32 v50, v50
	v_rcp_f32_e32 v51, v51
	v_pk_mul_f32 v[36:37], v[36:37], v[54:55] op_sel_hi:[1,0]
	v_rcp_f32_e32 v57, v53
	v_pk_mul_f32 v[36:37], v[40:41], v[36:37]
	v_pk_mul_f32 v[46:47], v[46:47], v[50:51]
	v_pk_mul_f32 v[36:37], v[36:37], v[48:49]
	s_waitcnt vmcnt(6)
	v_mov_b32_e32 v48, v137
	v_mov_b32_e32 v49, v138
	v_mov_b32_e32 v137, v139
	v_pk_add_f32 v[48:49], v[48:49], v[136:137]
	v_pk_mul_f32 v[40:41], v[42:43], v[52:53] op_sel_hi:[1,0]
	v_add_f32_e32 v50, v48, v49
	ds_bpermute_b32 v51, v172, v50
	v_exp_f32_e64 v42, -v40
	v_exp_f32_e64 v43, -v41
	v_pk_mul_f32 v[44:45], v[44:45], v[56:57]
	v_mov_b32_e32 v48, v3
	v_add_f32_e32 v42, 1.0, v42
	v_add_f32_e32 v43, 1.0, v43
	v_cvt_pk_fp8_f32 v48, v44, v45
	s_waitcnt lgkmcnt(0)
	v_add_f32_e32 v44, v50, v51
	v_rcp_f32_e32 v42, v42
	v_rcp_f32_e32 v43, v43
	v_mov_b32_e32 v49, v3
	ds_bpermute_b32 v45, v171, v44
	v_cvt_pk_fp8_f32 v49, v36, v37
	v_pk_mul_f32 v[38:39], v[38:39], v[54:55] op_sel_hi:[1,0]
	v_cvt_pk_fp8_f32 v48, v46, v47 op_sel:[0,0,1]
	v_pk_mul_f32 v[36:37], v[40:41], v[38:39]
	s_nop 0
	v_pk_mul_f32 v[36:37], v[36:37], v[42:43]
	s_nop 0
	v_cvt_pk_fp8_f32 v49, v36, v37 op_sel:[0,0,1]
	s_waitcnt lgkmcnt(0)
; __device__ __forceinline__ float rstd_fin4(const f32x4 a) { float s = (a[0] + a[1]) + (a[2] + a[3]); s += __shfl_xor(s, 16); s += __shfl_xor(s, 32); return __builtin_amdgcn_rsqf(s * (1.f / 1024.f) + 1e-6f); }
;     __device__ __forceinline__ void operator()(const f32x4 (&acc)[2][2][4][2], const Unit& u, int wr, int wc, int fr, int fq) const {
;     ...
;             for (int m = 0; m < 4; ++m) { const float rs = rstd_fin4(pa[ai][m]) * sc;
;                 const float rsl = rs * 1.4426950408889634f, rsu = rs * 0.6931471805599453f;
;                 f32x4 h0, h1;
; #pragma unroll
;                 for (int n = 0; n < 2; ++n) { const f32x4 G = acc[ai][0][m][n], U = acc[ai][1][m][n]; f32x4 hv;
; #pragma unroll
;                     for (int q = 0; q < 2; ++q) { const f32x2 g2 = (f32x2){G[2 * q], G[2 * q + 1]} * rsl, u2 = (f32x2){U[2 * q], U[2 * q + 1]} * rsu;
;                         f32x2 r2; r2.x = __builtin_amdgcn_rcpf(1.f + __builtin_amdgcn_exp2f(-g2.x)); r2.y = __builtin_amdgcn_rcpf(1.f + __builtin_amdgcn_exp2f(-g2.y));
;                         const f32x2 o2 = g2 * u2 * r2; hv[2 * q] = o2.x; hv[2 * q + 1] = o2.y; }
;                     if (n == 0) h0 = hv; else h1 = hv; }
;                 unsigned w0 = 0u, w1 = 0u;
;                 w0 = __builtin_amdgcn_cvt_pk_fp8_f32(h0[0], h0[1], w0, false); w0 = __builtin_amdgcn_cvt_pk_fp8_f32(h0[2], h0[3], w0, true); w1 = __builtin_amdgcn_cvt_pk_fp8_f32(h1[0], h1[1], w1, false); w1 = __builtin_amdgcn_cvt_pk_fp8_f32(h1[2], h1[3], w1, true);
;                 *(u32x2*)(hb + (ai * 4 + m) * 512) = (u32x2){w0, w1}; asm volatile("" ::: "memory"); }
	v_add_f32_e32 v36, v44, v45
	v_fmamk_f32 v36, v36, 0x3a800000, v227
	v_rsq_f32_e32 v37, v36
	global_store_dwordx2 v[166:167], v[48:49], off offset:2560 nt
	v_mul_f32_e32 v36, 0x3fb8aa3b, v37
	v_pk_mul_f32 v[32:33], v[32:33], v[36:37] op_sel_hi:[1,0]
	v_mul_f32_e32 v38, 0x3f317218, v37
	v_exp_f32_e64 v39, -v32
	v_exp_f32_e64 v37, -v33
	v_pk_mul_f32 v[28:29], v[28:29], v[38:39] op_sel_hi:[1,0]
	v_add_f32_e32 v37, 1.0, v37
	v_pk_mul_f32 v[28:29], v[32:33], v[28:29]
	v_pk_mul_f32 v[32:33], v[34:35], v[36:37] op_sel_hi:[1,0]
	v_add_f32_e32 v39, 1.0, v39
	v_exp_f32_e64 v34, -v32
	v_exp_f32_e64 v35, -v33
	v_pk_mul_f32 v[30:31], v[30:31], v[38:39] op_sel_hi:[1,0]
	v_pk_mul_f32 v[24:25], v[24:25], v[36:37] op_sel_hi:[1,0]
	v_add_f32_e32 v34, 1.0, v34
	v_add_f32_e32 v35, 1.0, v35
	v_pk_mul_f32 v[30:31], v[32:33], v[30:31]
	v_exp_f32_e64 v32, -v24
	v_exp_f32_e64 v33, -v25
	v_rcp_f32_e32 v34, v34
	v_rcp_f32_e32 v35, v35
	v_add_f32_e32 v32, 1.0, v32
	v_add_f32_e32 v33, 1.0, v33
	v_pk_mul_f32 v[26:27], v[26:27], v[36:37] op_sel_hi:[1,0]
	v_pk_mul_f32 v[30:31], v[30:31], v[34:35]
	v_rcp_f32_e32 v32, v32
	v_rcp_f32_e32 v33, v33
	v_exp_f32_e64 v34, -v26
	v_pk_mul_f32 v[20:21], v[20:21], v[38:39] op_sel_hi:[1,0]
	v_rcp_f32_e32 v40, v39
	v_pk_mul_f32 v[20:21], v[24:25], v[20:21]
	s_waitcnt vmcnt(6)
	v_mov_b32_e32 v24, v125
	v_mov_b32_e32 v25, v126
	v_mov_b32_e32 v125, v127
	v_pk_add_f32 v[24:25], v[24:25], v[124:125]
	v_pk_mul_f32 v[20:21], v[20:21], v[32:33]
	v_add_f32_e32 v32, 1.0, v34
	v_add_f32_e32 v34, v24, v25
	ds_bpermute_b32 v35, v172, v34
	v_exp_f32_e64 v33, -v27
	v_rcp_f32_e32 v24, v32
	v_rcp_f32_e32 v41, v37
	v_pk_mul_f32 v[22:23], v[22:23], v[38:39] op_sel_hi:[1,0]
	s_waitcnt lgkmcnt(0)
	v_add_f32_e32 v32, v34, v35
	v_add_f32_e32 v25, 1.0, v33
	ds_bpermute_b32 v33, v171, v32
	v_pk_mul_f32 v[22:23], v[26:27], v[22:23]
	v_mov_b32_e32 v27, v3
	v_cvt_pk_fp8_f32 v27, v20, v21
	v_pk_mul_f32 v[28:29], v[28:29], v[40:41]
	s_waitcnt lgkmcnt(0)
	v_add_f32_e32 v20, v32, v33
	v_rcp_f32_e32 v25, v25
	v_mov_b32_e32 v26, v3
	v_fmamk_f32 v20, v20, 0x3a800000, v227
	v_cvt_pk_fp8_f32 v26, v28, v29
	v_rsq_f32_e32 v28, v20
	v_pk_mul_f32 v[20:21], v[22:23], v[24:25]
	v_cvt_pk_fp8_f32 v26, v30, v31 op_sel:[0,0,1]
	v_cvt_pk_fp8_f32 v27, v20, v21 op_sel:[0,0,1]
	v_mul_f32_e32 v20, 0x3fb8aa3b, v28
	v_pk_mul_f32 v[16:17], v[16:17], v[20:21] op_sel_hi:[1,0]
	v_mul_f32_e32 v22, 0x3f317218, v28
	v_exp_f32_e64 v21, -v16
	v_exp_f32_e64 v23, -v17
	global_store_dwordx2 v[166:167], v[26:27], off offset:3072 nt
	v_add_f32_e32 v21, 1.0, v21
	v_pk_mul_f32 v[12:13], v[12:13], v[22:23] op_sel_hi:[1,0]
	v_rcp_f32_e32 v24, v21
	v_add_f32_e32 v21, 1.0, v23
	v_pk_mul_f32 v[12:13], v[16:17], v[12:13]
	v_pk_mul_f32 v[16:17], v[18:19], v[20:21] op_sel_hi:[1,0]
	v_pk_mul_f32 v[14:15], v[14:15], v[22:23] op_sel_hi:[1,0]
	v_pk_mul_f32 v[8:9], v[8:9], v[20:21] op_sel_hi:[1,0]
	v_exp_f32_e64 v18, -v16
	v_exp_f32_e64 v19, -v17
	v_pk_mul_f32 v[14:15], v[16:17], v[14:15]
	v_exp_f32_e64 v16, -v8
	v_exp_f32_e64 v17, -v9
	v_pk_mul_f32 v[4:5], v[4:5], v[22:23] op_sel_hi:[1,0]
	v_rcp_f32_e32 v25, v21
	v_pk_mul_f32 v[4:5], v[8:9], v[4:5]
	v_pk_mul_f32 v[8:9], v[10:11], v[20:21] op_sel_hi:[1,0]
	v_add_f32_e32 v16, 1.0, v16
	v_add_f32_e32 v17, 1.0, v17
	v_exp_f32_e64 v10, -v8
	v_exp_f32_e64 v11, -v9
	v_rcp_f32_e32 v16, v16
	v_rcp_f32_e32 v17, v17
	v_add_f32_e32 v18, 1.0, v18
	v_add_f32_e32 v19, 1.0, v19
	v_add_f32_e32 v10, 1.0, v10
	v_add_f32_e32 v11, 1.0, v11
	v_pk_mul_f32 v[12:13], v[12:13], v[24:25]
	v_rcp_f32_e32 v18, v18
	v_rcp_f32_e32 v19, v19
	v_pk_mul_f32 v[4:5], v[4:5], v[16:17]
	v_rcp_f32_e32 v10, v10
	v_rcp_f32_e32 v11, v11
	v_mov_b32_e32 v16, v3
	v_mov_b32_e32 v17, v3
	v_cvt_pk_fp8_f32 v16, v12, v13
	v_cvt_pk_fp8_f32 v17, v4, v5
	v_pk_mul_f32 v[6:7], v[6:7], v[22:23] op_sel_hi:[1,0]
	v_pk_mul_f32 v[14:15], v[14:15], v[18:19]
	v_pk_mul_f32 v[4:5], v[8:9], v[6:7]
	v_cvt_pk_fp8_f32 v16, v14, v15 op_sel:[0,0,1]
	v_pk_mul_f32 v[4:5], v[4:5], v[10:11]
	s_nop 0
	v_cvt_pk_fp8_f32 v17, v4, v5 op_sel:[0,0,1]
	global_store_dwordx2 v[166:167], v[16:17], off offset:3584 nt
	s_cbranch_vccnz .LBB0_1701
	s_andn2_b64 vcc, exec, s[46:47]
	s_cbranch_vccnz .LBB0_1700
	s_barrier
	s_branch .LBB0_1700
